# tail-converter bf16 weight stores write-through and non-temporal (sc1 nt) so the seam's L2 write-back has less to flush
# speedup vs baseline: 1.0078x; 1.0078x over previous
; __device__ __forceinline__ void conv_load(const ConvItem& ci, int lane, float (&v)[64]) {
;     ...
;     for (int i = 0; i < 64; ++i) { const int k = ci.k0 + i, kk = k < kmax ? k : kmax; v[i] = __builtin_nontemporal_load(base + (size_t)kk * ci.ldw); }
; #pragma unroll
;     for (int i = 0; i < 64; ++i) v[i] = (okc && (ci.k0 + i) < ci.Ksrc) ? v[i] : 0.f;
.Lcvp10_30:
	s_cmp_lt_i32 s58, s76
	s_cselect_b64 s[4:5], -1, 0
	s_and_b64 s[4:5], vcc, s[4:5]
	s_cmp_lt_i32 s64, s76
	s_waitcnt vmcnt(62)
	v_cndmask_b32_e64 v21, 0, v21, s[4:5]
	s_cselect_b64 s[4:5], -1, 0
	s_and_b64 s[4:5], vcc, s[4:5]
	s_cmp_lt_i32 s65, s76
	v_cndmask_b32_e64 v20, 0, v20, s[4:5]
	s_cselect_b64 s[4:5], -1, 0
	s_and_b64 s[4:5], vcc, s[4:5]
	s_cmp_lt_i32 s78, s76
	s_waitcnt vmcnt(61)
	v_cndmask_b32_e64 v19, 0, v19, s[4:5]
	s_cselect_b64 s[4:5], -1, 0
	s_and_b64 s[4:5], vcc, s[4:5]
	s_cmp_lt_i32 s79, s76
	s_waitcnt vmcnt(60)
	v_cndmask_b32_e64 v18, 0, v18, s[4:5]
	s_cselect_b64 s[4:5], -1, 0
	s_and_b64 s[4:5], vcc, s[4:5]
	s_cmp_lt_i32 s80, s76
	s_waitcnt vmcnt(59)
	v_cndmask_b32_e64 v17, 0, v17, s[4:5]
	s_cselect_b64 s[4:5], -1, 0
	s_and_b64 s[4:5], vcc, s[4:5]
	s_cmp_lt_i32 s81, s76
	s_waitcnt vmcnt(58)
	v_cndmask_b32_e64 v16, 0, v16, s[4:5]
	s_cselect_b64 s[4:5], -1, 0
	s_and_b64 s[4:5], vcc, s[4:5]
	s_cmp_lt_i32 s82, s76
	s_waitcnt vmcnt(57)
	v_cndmask_b32_e64 v15, 0, v15, s[4:5]
	s_cselect_b64 s[4:5], -1, 0
	s_and_b64 s[4:5], vcc, s[4:5]
	s_cmp_lt_i32 s83, s76
	s_waitcnt vmcnt(56)
	v_cndmask_b32_e64 v8, 0, v8, s[4:5]
	s_cselect_b64 s[4:5], -1, 0
	s_and_b64 s[4:5], vcc, s[4:5]
	s_cmp_lt_i32 s85, s76
	s_waitcnt vmcnt(55)
	v_cndmask_b32_e64 v29, 0, v29, s[4:5]
	s_cselect_b64 s[4:5], -1, 0
	s_and_b64 s[4:5], vcc, s[4:5]
	s_cmp_lt_i32 s86, s76
	s_waitcnt vmcnt(54)
	v_cndmask_b32_e64 v28, 0, v28, s[4:5]
	s_cselect_b64 s[4:5], -1, 0
	s_and_b64 s[4:5], vcc, s[4:5]
	s_cmp_lt_i32 s87, s76
	s_waitcnt vmcnt(53)
	v_cndmask_b32_e64 v27, 0, v27, s[4:5]
	s_cselect_b64 s[4:5], -1, 0
	s_and_b64 s[4:5], vcc, s[4:5]
	s_cmp_lt_i32 s88, s76
	s_waitcnt vmcnt(52)
	v_cndmask_b32_e64 v26, 0, v26, s[4:5]
	s_cselect_b64 s[4:5], -1, 0
	s_and_b64 s[4:5], vcc, s[4:5]
	s_cmp_lt_i32 s89, s76
	s_waitcnt vmcnt(51)
	v_cndmask_b32_e64 v25, 0, v25, s[4:5]
	s_cselect_b64 s[4:5], -1, 0
	s_and_b64 s[4:5], vcc, s[4:5]
	s_cmp_lt_i32 s90, s76
	s_waitcnt vmcnt(50)
	v_cndmask_b32_e64 v24, 0, v24, s[4:5]
	s_cselect_b64 s[4:5], -1, 0
	s_and_b64 s[4:5], vcc, s[4:5]
	s_cmp_lt_i32 s92, s76
	s_waitcnt vmcnt(49)
	v_cndmask_b32_e64 v23, 0, v23, s[4:5]
	s_cselect_b64 s[4:5], -1, 0
	s_and_b64 s[4:5], vcc, s[4:5]
	s_cmp_lt_i32 s93, s76
	s_waitcnt vmcnt(48)
	v_cndmask_b32_e64 v22, 0, v22, s[4:5]
	s_cselect_b64 s[4:5], -1, 0
	s_and_b64 s[4:5], vcc, s[4:5]
	s_cmp_lt_i32 s94, s76
	s_waitcnt vmcnt(47)
	v_cndmask_b32_e64 v37, 0, v37, s[4:5]
	s_cselect_b64 s[4:5], -1, 0
	s_and_b64 s[4:5], vcc, s[4:5]
	s_cmp_lt_i32 s95, s76
	s_waitcnt vmcnt(46)
	v_cndmask_b32_e64 v36, 0, v36, s[4:5]
	s_cselect_b64 s[4:5], -1, 0
	s_and_b64 s[4:5], vcc, s[4:5]
	s_cmp_lt_i32 s50, s76
	s_waitcnt vmcnt(45)
	v_cndmask_b32_e64 v35, 0, v35, s[4:5]
	s_cselect_b64 s[4:5], -1, 0
	s_and_b64 s[4:5], vcc, s[4:5]
	s_cmp_lt_i32 s51, s76
	s_waitcnt vmcnt(44)
	v_cndmask_b32_e64 v34, 0, v34, s[4:5]
	s_cselect_b64 s[4:5], -1, 0
	s_and_b64 s[4:5], vcc, s[4:5]
	s_cmp_lt_i32 s52, s76
	s_waitcnt vmcnt(43)
	v_cndmask_b32_e64 v33, 0, v33, s[4:5]
	s_cselect_b64 s[4:5], -1, 0
	s_and_b64 s[4:5], vcc, s[4:5]
	s_cmp_lt_i32 s53, s76
	s_waitcnt vmcnt(42)
	v_cndmask_b32_e64 v32, 0, v32, s[4:5]
	s_cselect_b64 s[4:5], -1, 0
	s_and_b64 s[4:5], vcc, s[4:5]
	s_cmp_lt_i32 s6, s76
	s_waitcnt vmcnt(41)
	v_cndmask_b32_e64 v31, 0, v31, s[4:5]
	s_cselect_b64 s[4:5], -1, 0
	s_and_b64 s[4:5], vcc, s[4:5]
	s_cmp_lt_i32 s7, s76
	s_waitcnt vmcnt(40)
	v_cndmask_b32_e64 v30, 0, v30, s[4:5]
	s_cselect_b64 s[4:5], -1, 0
	s_and_b64 s[4:5], vcc, s[4:5]
	s_cmp_lt_i32 s8, s76
	s_waitcnt vmcnt(39)
	v_cndmask_b32_e64 v45, 0, v45, s[4:5]
	s_cselect_b64 s[4:5], -1, 0
	s_and_b64 s[4:5], vcc, s[4:5]
	s_cmp_lt_i32 s9, s76
	s_waitcnt vmcnt(38)
	v_cndmask_b32_e64 v44, 0, v44, s[4:5]
	s_cselect_b64 s[4:5], -1, 0
	s_and_b64 s[4:5], vcc, s[4:5]
	s_cmp_lt_i32 s10, s76
	s_waitcnt vmcnt(37)
	v_cndmask_b32_e64 v43, 0, v43, s[4:5]
	s_cselect_b64 s[4:5], -1, 0
	s_and_b64 s[4:5], vcc, s[4:5]
	s_cmp_lt_i32 s11, s76
	s_waitcnt vmcnt(36)
	v_cndmask_b32_e64 v42, 0, v42, s[4:5]
	s_cselect_b64 s[4:5], -1, 0
	s_and_b64 s[4:5], vcc, s[4:5]
	s_cmp_lt_i32 s14, s76
	s_waitcnt vmcnt(35)
	v_cndmask_b32_e64 v41, 0, v41, s[4:5]
	s_cselect_b64 s[4:5], -1, 0
	s_and_b64 s[4:5], vcc, s[4:5]
	s_cmp_lt_i32 s15, s76
	s_waitcnt vmcnt(34)
	v_cndmask_b32_e64 v40, 0, v40, s[4:5]
	s_cselect_b64 s[4:5], -1, 0
	s_and_b64 s[4:5], vcc, s[4:5]
	s_cmp_lt_i32 s16, s76
	s_waitcnt vmcnt(33)
	v_cndmask_b32_e64 v39, 0, v39, s[4:5]
	s_cselect_b64 s[4:5], -1, 0
	s_and_b64 s[4:5], vcc, s[4:5]
	s_cmp_lt_i32 s17, s76
	s_waitcnt vmcnt(32)
	v_cndmask_b32_e64 v38, 0, v38, s[4:5]
	s_cselect_b64 s[4:5], -1, 0
	s_and_b64 s[4:5], vcc, s[4:5]
	s_cmp_lt_i32 s12, s76
	s_waitcnt vmcnt(31)
	v_cndmask_b32_e64 v53, 0, v53, s[4:5]
	s_cselect_b64 s[4:5], -1, 0
	s_and_b64 s[4:5], vcc, s[4:5]
	s_cmp_lt_i32 s13, s76
	s_waitcnt vmcnt(30)
	v_cndmask_b32_e64 v52, 0, v52, s[4:5]
	s_cselect_b64 s[4:5], -1, 0
	s_and_b64 s[4:5], vcc, s[4:5]
	s_cmp_lt_i32 s20, s76
	s_waitcnt vmcnt(29)
	v_cndmask_b32_e64 v51, 0, v51, s[4:5]
	s_cselect_b64 s[4:5], -1, 0
	s_and_b64 s[4:5], vcc, s[4:5]
	s_cmp_lt_i32 s21, s76
	s_waitcnt vmcnt(28)
	v_cndmask_b32_e64 v50, 0, v50, s[4:5]
	s_cselect_b64 s[4:5], -1, 0
	s_and_b64 s[4:5], vcc, s[4:5]
	s_cmp_lt_i32 s24, s76
	s_waitcnt vmcnt(27)
	v_cndmask_b32_e64 v49, 0, v49, s[4:5]
	s_cselect_b64 s[4:5], -1, 0
	s_and_b64 s[4:5], vcc, s[4:5]
	s_cmp_lt_i32 s25, s76
	s_waitcnt vmcnt(26)
	v_cndmask_b32_e64 v48, 0, v48, s[4:5]
	s_cselect_b64 s[4:5], -1, 0
	s_and_b64 s[4:5], vcc, s[4:5]
	s_cmp_lt_i32 s26, s76
	s_waitcnt vmcnt(25)
	v_cndmask_b32_e64 v47, 0, v47, s[4:5]
	s_cselect_b64 s[4:5], -1, 0
	s_and_b64 s[4:5], vcc, s[4:5]
	s_cmp_lt_i32 s27, s76
	s_waitcnt vmcnt(24)
; #define LAS __attribute__((address_space(3)))
; __device__ __forceinline__ void conv_load(const ConvItem& ci, int lane, float (&v)[64]) {
;     ...
;     for (int i = 0; i < 64; ++i) v[i] = (okc && (ci.k0 + i) < ci.Ksrc) ? v[i] : 0.f;
; }
; __device__ __forceinline__ void conv_store(const ConvItem& ci, LAS float* scr, int lane, const float (&v)[64]) {
;     const int c = lane & 7;
;     f32x4 s0 = {1.f, 1.f, 1.f, 1.f}, s1 = s0;
;     if (ci.ks) { const int kb = ci.k0 + 8 * c < ci.Ksrc - 8 ? ci.k0 + 8 * c : ci.Ksrc - 8; s0 = *(const f32x4*)(ci.ks + kb); s1 = *(const f32x4*)(ci.ks + kb + 4); }
; #pragma unroll
;     for (int i = 0; i < 64; ++i) scr[i * 65 + lane] = v[i];
	v_cndmask_b32_e64 v46, 0, v46, s[4:5]
	s_cselect_b64 s[4:5], -1, 0
	s_and_b64 s[4:5], vcc, s[4:5]
	s_cmp_lt_i32 s18, s76
	s_waitcnt vmcnt(23)
	v_cndmask_b32_e64 v61, 0, v61, s[4:5]
	s_cselect_b64 s[4:5], -1, 0
	s_and_b64 s[4:5], vcc, s[4:5]
	s_cmp_lt_i32 s19, s76
	s_waitcnt vmcnt(22)
	v_cndmask_b32_e64 v60, 0, v60, s[4:5]
	s_cselect_b64 s[4:5], -1, 0
	s_and_b64 s[4:5], vcc, s[4:5]
	s_cmp_lt_i32 s28, s76
	s_waitcnt vmcnt(21)
	v_cndmask_b32_e64 v59, 0, v59, s[4:5]
	s_cselect_b64 s[4:5], -1, 0
	s_and_b64 s[4:5], vcc, s[4:5]
	s_cmp_lt_i32 s29, s76
	s_waitcnt vmcnt(20)
	v_cndmask_b32_e64 v58, 0, v58, s[4:5]
	s_cselect_b64 s[4:5], -1, 0
	s_and_b64 s[4:5], vcc, s[4:5]
	s_cmp_lt_i32 s22, s76
	s_waitcnt vmcnt(19)
	v_cndmask_b32_e64 v57, 0, v57, s[4:5]
	s_cselect_b64 s[4:5], -1, 0
	s_and_b64 s[4:5], vcc, s[4:5]
	s_cmp_lt_i32 s23, s76
	s_waitcnt vmcnt(18)
	v_cndmask_b32_e64 v56, 0, v56, s[4:5]
	s_cselect_b64 s[4:5], -1, 0
	s_and_b64 s[4:5], vcc, s[4:5]
	s_cmp_lt_i32 s30, s76
	s_waitcnt vmcnt(17)
	v_cndmask_b32_e64 v55, 0, v55, s[4:5]
	s_cselect_b64 s[4:5], -1, 0
	s_and_b64 s[4:5], vcc, s[4:5]
	s_cmp_lt_i32 s31, s76
	s_waitcnt vmcnt(16)
	v_cndmask_b32_e64 v54, 0, v54, s[4:5]
	s_cselect_b64 s[4:5], -1, 0
	s_and_b64 s[4:5], vcc, s[4:5]
	s_cmp_lt_i32 s36, s76
	s_waitcnt vmcnt(15)
	v_cndmask_b32_e64 v70, 0, v70, s[4:5]
	s_cselect_b64 s[4:5], -1, 0
	s_and_b64 s[4:5], vcc, s[4:5]
	s_cmp_lt_i32 s37, s76
	s_waitcnt vmcnt(14)
	v_cndmask_b32_e64 v69, 0, v69, s[4:5]
	s_cselect_b64 s[4:5], -1, 0
	s_and_b64 s[4:5], vcc, s[4:5]
	s_cmp_lt_i32 s38, s76
	s_waitcnt vmcnt(13)
	v_cndmask_b32_e64 v68, 0, v68, s[4:5]
	s_cselect_b64 s[4:5], -1, 0
	s_and_b64 s[4:5], vcc, s[4:5]
	s_cmp_lt_i32 s39, s76
	s_waitcnt vmcnt(12)
	v_cndmask_b32_e64 v67, 0, v67, s[4:5]
	s_cselect_b64 s[4:5], -1, 0
	s_and_b64 s[4:5], vcc, s[4:5]
	s_cmp_lt_i32 s34, s76
	s_waitcnt vmcnt(11)
	v_cndmask_b32_e64 v66, 0, v66, s[4:5]
	s_cselect_b64 s[4:5], -1, 0
	s_and_b64 s[4:5], vcc, s[4:5]
	s_cmp_lt_i32 s35, s76
	s_waitcnt vmcnt(10)
	v_cndmask_b32_e64 v64, 0, v64, s[4:5]
	s_cselect_b64 s[4:5], -1, 0
	s_and_b64 s[4:5], vcc, s[4:5]
	s_cmp_lt_i32 s42, s76
	s_waitcnt vmcnt(9)
	v_cndmask_b32_e64 v63, 0, v63, s[4:5]
	s_cselect_b64 s[4:5], -1, 0
	s_and_b64 s[4:5], vcc, s[4:5]
	s_cmp_lt_i32 s43, s76
	s_waitcnt vmcnt(8)
	v_cndmask_b32_e64 v62, 0, v62, s[4:5]
	s_cselect_b64 s[4:5], -1, 0
	s_and_b64 s[4:5], vcc, s[4:5]
	s_cmp_lt_i32 s54, s76
	s_waitcnt vmcnt(7)
	v_cndmask_b32_e64 v65, 0, v65, s[4:5]
	s_cselect_b64 s[4:5], -1, 0
	s_and_b64 s[4:5], vcc, s[4:5]
	s_cmp_lt_i32 s55, s76
	s_waitcnt vmcnt(6)
	v_cndmask_b32_e64 v74, 0, v74, s[4:5]
	s_cselect_b64 s[4:5], -1, 0
	s_and_b64 s[4:5], vcc, s[4:5]
	s_cmp_lt_i32 s46, s76
	ds_write2_b32 v12, v21, v20 offset1:65
	ds_write2_b32 v12, v19, v18 offset0:130 offset1:195
	v_add_u32_e32 v18, 0x400, v12
	s_waitcnt vmcnt(5)
	v_cndmask_b32_e64 v73, 0, v73, s[4:5]
	s_cselect_b64 s[4:5], -1, 0
	ds_write2_b32 v18, v17, v16 offset0:4 offset1:69
	ds_write2_b32 v18, v15, v8 offset0:134 offset1:199
	v_add_u32_e32 v8, 0x800, v12
	s_and_b64 s[4:5], vcc, s[4:5]
	ds_write2_b32 v8, v29, v28 offset0:8 offset1:73
	ds_write2_b32 v8, v27, v26 offset0:138 offset1:203
	v_add_u32_e32 v8, 0xc00, v12
	s_cmp_lt_i32 s47, s76
	ds_write2_b32 v8, v25, v24 offset0:12 offset1:77
	ds_write2_b32 v8, v23, v22 offset0:142 offset1:207
	v_add_u32_e32 v8, 0x1000, v12
	s_waitcnt vmcnt(4)
	v_cndmask_b32_e64 v72, 0, v72, s[4:5]
	s_cselect_b64 s[4:5], -1, 0
	ds_write2_b32 v8, v37, v36 offset0:16 offset1:81
	ds_write2_b32 v8, v35, v34 offset0:146 offset1:211
	v_add_u32_e32 v8, 0x1400, v12
	s_and_b64 s[4:5], vcc, s[4:5]
	ds_write2_b32 v8, v33, v32 offset0:20 offset1:85
	ds_write2_b32 v8, v31, v30 offset0:150 offset1:215
	v_add_u32_e32 v8, 0x1800, v12
	s_cmp_lt_i32 s48, s76
	ds_write2_b32 v8, v45, v44 offset0:24 offset1:89
	ds_write2_b32 v8, v43, v42 offset0:154 offset1:219
	v_add_u32_e32 v8, 0x1c00, v12
	s_waitcnt vmcnt(3)
	v_cndmask_b32_e64 v71, 0, v71, s[4:5]
	s_cselect_b64 s[4:5], -1, 0
	ds_write2_b32 v8, v41, v40 offset0:28 offset1:93
	ds_write2_b32 v8, v39, v38 offset0:158 offset1:223
	v_add_u32_e32 v8, 0x2000, v12
	s_and_b64 s[4:5], vcc, s[4:5]
	ds_write2_b32 v8, v53, v52 offset0:32 offset1:97
	ds_write2_b32 v8, v51, v50 offset0:162 offset1:227
	v_add_u32_e32 v8, 0x2400, v12
	s_cmp_lt_i32 s49, s76
	ds_write2_b32 v8, v49, v48 offset0:36 offset1:101
	ds_write2_b32 v8, v47, v46 offset0:166 offset1:231
	v_add_u32_e32 v8, 0x2800, v12
	s_waitcnt vmcnt(2)
	v_cndmask_b32_e64 v77, 0, v77, s[4:5]
	s_cselect_b64 s[4:5], -1, 0
	ds_write2_b32 v8, v61, v60 offset0:40 offset1:105
	ds_write2_b32 v8, v59, v58 offset0:170 offset1:235
	v_add_u32_e32 v8, 0x2c00, v12
	s_and_b64 s[4:5], vcc, s[4:5]
	ds_write2_b32 v8, v57, v56 offset0:44 offset1:109
	ds_write2_b32 v8, v55, v54 offset0:174 offset1:239
	v_add_u32_e32 v8, 0x3000, v12
	s_cmp_lt_i32 s44, s76
	ds_write2_b32 v8, v70, v69 offset0:48 offset1:113
	ds_write2_b32 v8, v68, v67 offset0:178 offset1:243
	v_add_u32_e32 v8, 0x3400, v12
	s_waitcnt vmcnt(1)
	v_cndmask_b32_e64 v76, 0, v76, s[4:5]
	s_cselect_b64 s[4:5], -1, 0
	ds_write2_b32 v8, v66, v64 offset0:52 offset1:117
	ds_write2_b32 v8, v63, v62 offset0:182 offset1:247
	v_add_u32_e32 v8, 0x3800, v12
	s_and_b64 vcc, vcc, s[4:5]
	ds_write2_b32 v8, v65, v74 offset0:56 offset1:121
	ds_write2_b32 v8, v73, v72 offset0:186 offset1:251
	v_add_u32_e32 v8, 0x3c00, v12
	s_waitcnt vmcnt(0)
	v_cndmask_b32_e32 v75, 0, v75, vcc
	ds_write2_b32 v8, v71, v77 offset0:60 offset1:125
	ds_write2_b32 v8, v76, v75 offset0:190 offset1:255
	s_waitcnt lgkmcnt(0)
; __device__ __forceinline__ unsigned cvt_pk_bf16(float lo, float hi) { unsigned r; asm volatile("v_cvt_pk_bf16_f32 %0, %1, %2" : "=v"(r) : "v"(lo), "v"(hi)); return r; }
; #define LAS __attribute__((address_space(3)))
; __device__ __forceinline__ void conv_store(const ConvItem& ci, LAS float* scr, int lane, const float (&v)[64]) {
;     ...
;     for (int j = 0; j < 8; ++j) { const int n = (lane >> 3) + 8 * j; const LAS float* s = scr + (8 * c) * 65 + n;
;         v4u o; o.x = cvt_pk_bf16(s[0 * 65] * s0[0], s[1 * 65] * s0[1]); o.y = cvt_pk_bf16(s[2 * 65] * s0[2], s[3 * 65] * s0[3]); o.z = cvt_pk_bf16(s[4 * 65] * s1[0], s[5 * 65] * s1[1]); o.w = cvt_pk_bf16(s[6 * 65] * s1[2], s[7 * 65] * s1[3]);
;         *(v4u*)(ci.dst + (size_t)(ci.drow0 + n) * ci.ldd + ci.k0 + 8 * c) = o; }
	v_add_u32_e32 v192, 0x400, v14
	ds_read2_b32 v[128:129], v14 offset1:65
	ds_read2_b32 v[130:131], v14 offset0:130 offset1:195
	ds_read2_b32 v[132:133], v192 offset0:4 offset1:69
	ds_read2_b32 v[134:135], v192 offset0:134 offset1:199
	ds_read2_b32 v[136:137], v14 offset0:8 offset1:73
	ds_read2_b32 v[138:139], v14 offset0:138 offset1:203
	ds_read2_b32 v[140:141], v192 offset0:12 offset1:77
	ds_read2_b32 v[142:143], v192 offset0:142 offset1:207
	ds_read2_b32 v[144:145], v14 offset0:16 offset1:81
	ds_read2_b32 v[146:147], v14 offset0:146 offset1:211
	ds_read2_b32 v[148:149], v192 offset0:20 offset1:85
	ds_read2_b32 v[150:151], v192 offset0:150 offset1:215
	ds_read2_b32 v[152:153], v14 offset0:24 offset1:89
	ds_read2_b32 v[154:155], v14 offset0:154 offset1:219
	ds_read2_b32 v[156:157], v192 offset0:28 offset1:93
	ds_read2_b32 v[158:159], v192 offset0:158 offset1:223
	ds_read2_b32 v[160:161], v14 offset0:32 offset1:97
	ds_read2_b32 v[162:163], v14 offset0:162 offset1:227
	ds_read2_b32 v[164:165], v192 offset0:36 offset1:101
	ds_read2_b32 v[166:167], v192 offset0:166 offset1:231
	ds_read2_b32 v[168:169], v14 offset0:40 offset1:105
	ds_read2_b32 v[170:171], v14 offset0:170 offset1:235
	ds_read2_b32 v[172:173], v192 offset0:44 offset1:109
	ds_read2_b32 v[174:175], v192 offset0:174 offset1:239
	ds_read2_b32 v[176:177], v14 offset0:48 offset1:113
	ds_read2_b32 v[178:179], v14 offset0:178 offset1:243
	ds_read2_b32 v[180:181], v192 offset0:52 offset1:117
	ds_read2_b32 v[182:183], v192 offset0:182 offset1:247
	ds_read2_b32 v[184:185], v14 offset0:56 offset1:121
	ds_read2_b32 v[186:187], v14 offset0:186 offset1:251
	ds_read2_b32 v[188:189], v192 offset0:60 offset1:125
	ds_read2_b32 v[190:191], v192 offset0:190 offset1:255
	s_waitcnt lgkmcnt(0)
	v_add_u32_e32 v24, s59, v13
	v_mul_lo_u32 v22, s57, v24
	s_ashr_i32 s59, s58, 31
	v_readlane_b32 s76, v254, 31
	s_waitcnt lgkmcnt(0)
	v_mul_f32_e32 v8, v4, v128
	v_mul_f32_e32 v15, v5, v129
	v_cvt_pk_bf16_f32 v16, v8, v15
	s_add_i32 s3, s3, s33
	s_add_i32 s66, s66, s67
	s_add_i32 s68, s68, s69
	s_add_i32 s70, s70, s71
	s_waitcnt lgkmcnt(0)
	v_mul_f32_e32 v15, v7, v131
	v_mul_f32_e32 v8, v6, v130
	v_cvt_pk_bf16_f32 v17, v8, v15
	v_add_u32_e32 v15, 0x400, v14
	s_add_i32 s72, s72, s73
	s_add_i32 s74, s74, s75
	v_readlane_b32 s78, v254, 33
	v_readlane_b32 s79, v254, 34
	s_waitcnt lgkmcnt(0)
	v_mul_f32_e32 v8, v0, v132
	v_mul_f32_e32 v18, v1, v133
	v_cvt_pk_bf16_f32 v18, v8, v18
	v_readlane_b32 s80, v255, 21
	v_readlane_b32 s77, v254, 32
	s_movk_i32 s78, 0x1580
	v_readlane_b32 s82, v255, 23
	s_waitcnt lgkmcnt(0)
	v_mul_f32_e32 v8, v2, v134
	v_mul_f32_e32 v19, v3, v135
	v_cvt_pk_bf16_f32 v19, v8, v19
	v_ashrrev_i32_e32 v8, 31, v24
	v_mul_lo_u32 v8, s56, v8
	v_mad_u64_u32 v[20:21], s[4:5], s56, v24, 0
	v_add3_u32 v21, v21, v8, v22
	v_lshl_add_u64 v[20:21], v[20:21], 1, s[60:61]
	s_lshl_b64 s[4:5], s[58:59], 1
	v_lshl_add_u64 v[20:21], v[20:21], 0, s[4:5]
	v_lshlrev_b32_e32 v8, 1, v10
	v_lshl_add_u64 v[20:21], v[20:21], 0, v[8:9]
	global_store_dwordx4 v[20:21], v[16:19], off sc1 nt
	s_cmpk_lt_i32 s3, 11008
	v_readlane_b32 s83, v255, 24
	s_waitcnt lgkmcnt(0)
	v_mul_f32_e32 v16, v4, v136
	v_mul_f32_e32 v17, v5, v137
	v_cvt_pk_bf16_f32 v16, v16, v17
	s_mov_b32 s79, 0x3f22f983
	s_mov_b32 s85, 0xbfc90fda
	s_brev_b32 s86, 1
	s_movk_i32 s87, 0x1f8
	s_waitcnt lgkmcnt(0)
	v_mul_f32_e32 v17, v6, v138
	v_mul_f32_e32 v18, v7, v139
	v_cvt_pk_bf16_f32 v17, v17, v18
	s_mov_b64 s[88:89], 0x80
	s_mov_b64 s[92:93], 0x4000
	s_mov_b64 s[94:95], 0x4800
	v_readlane_b32 s81, v255, 22
	s_waitcnt lgkmcnt(0)
	v_mul_f32_e32 v18, v0, v140
	v_mul_f32_e32 v19, v1, v141
	v_cvt_pk_bf16_f32 v18, v18, v19
	s_waitcnt lgkmcnt(0)
	v_mul_f32_e32 v19, v2, v142
	v_mul_f32_e32 v20, v3, v143
	v_cvt_pk_bf16_f32 v19, v19, v20
	v_add_u32_e32 v20, 8, v24
	v_ashrrev_i32_e32 v21, 31, v20
	v_mul_lo_u32 v22, s56, v21
	v_mul_lo_u32 v23, s57, v20
	v_mad_u64_u32 v[20:21], s[6:7], s56, v20, 0
	v_add3_u32 v21, v21, v22, v23
	v_lshl_add_u64 v[20:21], v[20:21], 1, s[60:61]
	v_lshl_add_u64 v[20:21], v[20:21], 0, s[4:5]
	v_lshl_add_u64 v[20:21], v[20:21], 0, v[8:9]
	global_store_dwordx4 v[20:21], v[16:19], off sc1 nt
	s_waitcnt lgkmcnt(0)
	s_nop 0
	v_mul_f32_e32 v16, v4, v144
	v_mul_f32_e32 v17, v5, v145
	v_cvt_pk_bf16_f32 v16, v16, v17
	s_waitcnt lgkmcnt(0)
	v_mul_f32_e32 v17, v6, v146
	v_mul_f32_e32 v18, v7, v147
	v_cvt_pk_bf16_f32 v17, v17, v18
	s_waitcnt lgkmcnt(0)
	v_mul_f32_e32 v18, v0, v148
	v_mul_f32_e32 v19, v1, v149
	v_cvt_pk_bf16_f32 v18, v18, v19
	s_waitcnt lgkmcnt(0)
; __device__ __forceinline__ unsigned cvt_pk_bf16(float lo, float hi) { unsigned r; asm volatile("v_cvt_pk_bf16_f32 %0, %1, %2" : "=v"(r) : "v"(lo), "v"(hi)); return r; }
; #define LAS __attribute__((address_space(3)))
; __device__ __forceinline__ void conv_store(const ConvItem& ci, LAS float* scr, int lane, const float (&v)[64]) {
;     ...
;     for (int j = 0; j < 8; ++j) { const int n = (lane >> 3) + 8 * j; const LAS float* s = scr + (8 * c) * 65 + n;
;         v4u o; o.x = cvt_pk_bf16(s[0 * 65] * s0[0], s[1 * 65] * s0[1]); o.y = cvt_pk_bf16(s[2 * 65] * s0[2], s[3 * 65] * s0[3]); o.z = cvt_pk_bf16(s[4 * 65] * s1[0], s[5 * 65] * s1[1]); o.w = cvt_pk_bf16(s[6 * 65] * s1[2], s[7 * 65] * s1[3]);
;         *(v4u*)(ci.dst + (size_t)(ci.drow0 + n) * ci.ldd + ci.k0 + 8 * c) = o; }
	v_mul_f32_e32 v19, v2, v150
	v_mul_f32_e32 v20, v3, v151
	v_cvt_pk_bf16_f32 v19, v19, v20
	v_add_u32_e32 v20, 16, v24
	v_ashrrev_i32_e32 v21, 31, v20
	v_mul_lo_u32 v22, s56, v21
	v_mul_lo_u32 v23, s57, v20
	v_mad_u64_u32 v[20:21], s[6:7], s56, v20, 0
	v_add3_u32 v21, v21, v22, v23
	v_lshl_add_u64 v[20:21], v[20:21], 1, s[60:61]
	v_lshl_add_u64 v[20:21], v[20:21], 0, s[4:5]
	v_lshl_add_u64 v[20:21], v[20:21], 0, v[8:9]
	global_store_dwordx4 v[20:21], v[16:19], off sc1 nt
	s_waitcnt lgkmcnt(0)
	s_nop 0
	v_mul_f32_e32 v16, v4, v152
	v_mul_f32_e32 v17, v5, v153
	v_cvt_pk_bf16_f32 v16, v16, v17
	s_waitcnt lgkmcnt(0)
	v_mul_f32_e32 v17, v6, v154
	v_mul_f32_e32 v18, v7, v155
	v_cvt_pk_bf16_f32 v17, v17, v18
	s_waitcnt lgkmcnt(0)
	v_mul_f32_e32 v18, v0, v156
	v_mul_f32_e32 v19, v1, v157
	v_cvt_pk_bf16_f32 v18, v18, v19
	s_waitcnt lgkmcnt(0)
	v_mul_f32_e32 v19, v2, v158
	v_mul_f32_e32 v20, v3, v159
	v_cvt_pk_bf16_f32 v19, v19, v20
	v_add_u32_e32 v20, 24, v24
	v_ashrrev_i32_e32 v21, 31, v20
	v_mul_lo_u32 v22, s56, v21
	v_mul_lo_u32 v23, s57, v20
	v_mad_u64_u32 v[20:21], s[6:7], s56, v20, 0
	v_add3_u32 v21, v21, v22, v23
	v_lshl_add_u64 v[20:21], v[20:21], 1, s[60:61]
	v_lshl_add_u64 v[20:21], v[20:21], 0, s[4:5]
	v_lshl_add_u64 v[20:21], v[20:21], 0, v[8:9]
	global_store_dwordx4 v[20:21], v[16:19], off sc1 nt
	s_waitcnt lgkmcnt(0)
	s_nop 0
	v_mul_f32_e32 v16, v4, v160
	v_mul_f32_e32 v17, v5, v161
	v_cvt_pk_bf16_f32 v16, v16, v17
	s_waitcnt lgkmcnt(0)
	v_mul_f32_e32 v17, v6, v162
	v_mul_f32_e32 v18, v7, v163
	v_cvt_pk_bf16_f32 v17, v17, v18
	s_waitcnt lgkmcnt(0)
	v_mul_f32_e32 v18, v0, v164
	v_mul_f32_e32 v19, v1, v165
	v_cvt_pk_bf16_f32 v18, v18, v19
	s_waitcnt lgkmcnt(0)
	v_mul_f32_e32 v19, v2, v166
	v_mul_f32_e32 v20, v3, v167
	v_cvt_pk_bf16_f32 v19, v19, v20
	v_add_u32_e32 v20, 32, v24
	v_ashrrev_i32_e32 v21, 31, v20
	v_mul_lo_u32 v22, s56, v21
	v_mul_lo_u32 v23, s57, v20
	v_mad_u64_u32 v[20:21], s[6:7], s56, v20, 0
	v_add3_u32 v21, v21, v22, v23
	v_lshl_add_u64 v[20:21], v[20:21], 1, s[60:61]
	v_lshl_add_u64 v[20:21], v[20:21], 0, s[4:5]
	v_lshl_add_u64 v[20:21], v[20:21], 0, v[8:9]
	global_store_dwordx4 v[20:21], v[16:19], off sc1 nt
	s_waitcnt lgkmcnt(0)
	s_nop 0
	v_mul_f32_e32 v16, v4, v168
	v_mul_f32_e32 v17, v5, v169
	v_cvt_pk_bf16_f32 v16, v16, v17
	s_waitcnt lgkmcnt(0)
	v_mul_f32_e32 v17, v6, v170
	v_mul_f32_e32 v18, v7, v171
	v_cvt_pk_bf16_f32 v17, v17, v18
	s_waitcnt lgkmcnt(0)
	v_mul_f32_e32 v18, v0, v172
	v_mul_f32_e32 v19, v1, v173
	v_cvt_pk_bf16_f32 v18, v18, v19
	s_waitcnt lgkmcnt(0)
	v_mul_f32_e32 v19, v2, v174
	v_mul_f32_e32 v20, v3, v175
	v_cvt_pk_bf16_f32 v19, v19, v20
	v_add_u32_e32 v20, 40, v24
	v_ashrrev_i32_e32 v21, 31, v20
	v_mul_lo_u32 v22, s56, v21
	v_mul_lo_u32 v23, s57, v20
	v_mad_u64_u32 v[20:21], s[6:7], s56, v20, 0
	v_add3_u32 v21, v21, v22, v23
	v_lshl_add_u64 v[20:21], v[20:21], 1, s[60:61]
	v_lshl_add_u64 v[20:21], v[20:21], 0, s[4:5]
	v_lshl_add_u64 v[20:21], v[20:21], 0, v[8:9]
	global_store_dwordx4 v[20:21], v[16:19], off sc1 nt
	s_waitcnt lgkmcnt(0)
	s_nop 0
	v_mul_f32_e32 v16, v4, v176
	v_mul_f32_e32 v17, v5, v177
	v_cvt_pk_bf16_f32 v16, v16, v17
	s_waitcnt lgkmcnt(0)
	v_mul_f32_e32 v17, v6, v178
	v_mul_f32_e32 v18, v7, v179
	v_cvt_pk_bf16_f32 v17, v17, v18
	s_waitcnt lgkmcnt(0)
	v_mul_f32_e32 v18, v0, v180
	v_mul_f32_e32 v19, v1, v181
	v_cvt_pk_bf16_f32 v18, v18, v19
	s_waitcnt lgkmcnt(0)
	v_mul_f32_e32 v19, v2, v182
	v_mul_f32_e32 v20, v3, v183
	v_cvt_pk_bf16_f32 v19, v19, v20
	v_add_u32_e32 v20, 48, v24
	v_ashrrev_i32_e32 v21, 31, v20
	v_mul_lo_u32 v22, s56, v21
	v_mul_lo_u32 v23, s57, v20
	v_mad_u64_u32 v[20:21], s[6:7], s56, v20, 0
	v_add3_u32 v21, v21, v22, v23
	v_lshl_add_u64 v[20:21], v[20:21], 1, s[60:61]
	v_lshl_add_u64 v[20:21], v[20:21], 0, s[4:5]
	v_lshl_add_u64 v[20:21], v[20:21], 0, v[8:9]
	global_store_dwordx4 v[20:21], v[16:19], off sc1 nt
	s_waitcnt lgkmcnt(0)
	v_mul_f32_e32 v4, v4, v184
	v_mul_f32_e32 v5, v5, v185
	v_cvt_pk_bf16_f32 v4, v4, v5
	s_waitcnt lgkmcnt(0)
	v_mul_f32_e32 v5, v6, v186
	v_mul_f32_e32 v6, v7, v187
	v_cvt_pk_bf16_f32 v5, v5, v6
	s_waitcnt lgkmcnt(0)
	v_mul_f32_e32 v0, v0, v188
	v_mul_f32_e32 v1, v1, v189
	v_cvt_pk_bf16_f32 v6, v0, v1
	s_waitcnt lgkmcnt(0)
	v_mul_f32_e32 v0, v2, v190
	v_mul_f32_e32 v1, v3, v191
	v_cvt_pk_bf16_f32 v7, v0, v1
	v_add_u32_e32 v0, 56, v24
	v_ashrrev_i32_e32 v1, 31, v0
	v_mul_lo_u32 v2, s56, v1
	v_mul_lo_u32 v3, s57, v0
	v_mad_u64_u32 v[0:1], s[6:7], s56, v0, 0
	v_add3_u32 v1, v1, v2, v3
	v_lshl_add_u64 v[0:1], v[0:1], 1, s[60:61]
	v_lshl_add_u64 v[0:1], v[0:1], 0, s[4:5]
	v_lshl_add_u64 v[0:1], v[0:1], 0, v[8:9]
	global_store_dwordx4 v[0:1], v[4:7], off sc1 nt
	s_waitcnt lgkmcnt(0)
	s_cbranch_scc0 .Lcvp10_ret

; __device__ __forceinline__ void conv_load(const ConvItem& ci, int lane, float (&v)[64]) {
;     ...
;     for (int i = 0; i < 64; ++i) v[i] = (okc && (ci.k0 + i) < ci.Ksrc) ? v[i] : 0.f;
.Lcvp11_30:
	s_cmp_lt_i32 s58, s76
	s_cselect_b64 s[4:5], -1, 0
	s_and_b64 s[4:5], vcc, s[4:5]
	s_cmp_lt_i32 s64, s76
	s_waitcnt vmcnt(62)
	v_cndmask_b32_e64 v21, 0, v21, s[4:5]
	s_cselect_b64 s[4:5], -1, 0
	s_and_b64 s[4:5], vcc, s[4:5]
	s_cmp_lt_i32 s65, s76
	v_cndmask_b32_e64 v20, 0, v20, s[4:5]
	s_cselect_b64 s[4:5], -1, 0
	s_and_b64 s[4:5], vcc, s[4:5]
	s_cmp_lt_i32 s78, s76
	s_waitcnt vmcnt(61)
	v_cndmask_b32_e64 v19, 0, v19, s[4:5]
	s_cselect_b64 s[4:5], -1, 0
	s_and_b64 s[4:5], vcc, s[4:5]
	s_cmp_lt_i32 s79, s76
	s_waitcnt vmcnt(60)
	v_cndmask_b32_e64 v18, 0, v18, s[4:5]
	s_cselect_b64 s[4:5], -1, 0
	s_and_b64 s[4:5], vcc, s[4:5]
	s_cmp_lt_i32 s80, s76
	s_waitcnt vmcnt(59)
	v_cndmask_b32_e64 v17, 0, v17, s[4:5]
	s_cselect_b64 s[4:5], -1, 0
	s_and_b64 s[4:5], vcc, s[4:5]
	s_cmp_lt_i32 s81, s76
	s_waitcnt vmcnt(58)
	v_cndmask_b32_e64 v16, 0, v16, s[4:5]
	s_cselect_b64 s[4:5], -1, 0
	s_and_b64 s[4:5], vcc, s[4:5]
	s_cmp_lt_i32 s82, s76
	s_waitcnt vmcnt(57)
	v_cndmask_b32_e64 v15, 0, v15, s[4:5]
	s_cselect_b64 s[4:5], -1, 0
	s_and_b64 s[4:5], vcc, s[4:5]
	s_cmp_lt_i32 s83, s76
	s_waitcnt vmcnt(56)
	v_cndmask_b32_e64 v8, 0, v8, s[4:5]
	s_cselect_b64 s[4:5], -1, 0
	s_and_b64 s[4:5], vcc, s[4:5]
	s_cmp_lt_i32 s85, s76
	s_waitcnt vmcnt(55)
	v_cndmask_b32_e64 v29, 0, v29, s[4:5]
	s_cselect_b64 s[4:5], -1, 0
	s_and_b64 s[4:5], vcc, s[4:5]
	s_cmp_lt_i32 s86, s76
	s_waitcnt vmcnt(54)
	v_cndmask_b32_e64 v28, 0, v28, s[4:5]
	s_cselect_b64 s[4:5], -1, 0
	s_and_b64 s[4:5], vcc, s[4:5]
	s_cmp_lt_i32 s87, s76
	s_waitcnt vmcnt(53)
	v_cndmask_b32_e64 v27, 0, v27, s[4:5]
	s_cselect_b64 s[4:5], -1, 0
	s_and_b64 s[4:5], vcc, s[4:5]
	s_cmp_lt_i32 s88, s76
	s_waitcnt vmcnt(52)
	v_cndmask_b32_e64 v26, 0, v26, s[4:5]
	s_cselect_b64 s[4:5], -1, 0
	s_and_b64 s[4:5], vcc, s[4:5]
	s_cmp_lt_i32 s89, s76
	s_waitcnt vmcnt(51)
	v_cndmask_b32_e64 v25, 0, v25, s[4:5]
	s_cselect_b64 s[4:5], -1, 0
	s_and_b64 s[4:5], vcc, s[4:5]
	s_cmp_lt_i32 s90, s76
	s_waitcnt vmcnt(50)
	v_cndmask_b32_e64 v24, 0, v24, s[4:5]
	s_cselect_b64 s[4:5], -1, 0
	s_and_b64 s[4:5], vcc, s[4:5]
	s_cmp_lt_i32 s92, s76
	s_waitcnt vmcnt(49)
	v_cndmask_b32_e64 v23, 0, v23, s[4:5]
	s_cselect_b64 s[4:5], -1, 0
	s_and_b64 s[4:5], vcc, s[4:5]
	s_cmp_lt_i32 s93, s76
	s_waitcnt vmcnt(48)
	v_cndmask_b32_e64 v22, 0, v22, s[4:5]
	s_cselect_b64 s[4:5], -1, 0
	s_and_b64 s[4:5], vcc, s[4:5]
	s_cmp_lt_i32 s94, s76
	s_waitcnt vmcnt(47)
	v_cndmask_b32_e64 v37, 0, v37, s[4:5]
	s_cselect_b64 s[4:5], -1, 0
	s_and_b64 s[4:5], vcc, s[4:5]
	s_cmp_lt_i32 s95, s76
	s_waitcnt vmcnt(46)
	v_cndmask_b32_e64 v36, 0, v36, s[4:5]
	s_cselect_b64 s[4:5], -1, 0
	s_and_b64 s[4:5], vcc, s[4:5]
	s_cmp_lt_i32 s50, s76
	s_waitcnt vmcnt(45)
	v_cndmask_b32_e64 v35, 0, v35, s[4:5]
	s_cselect_b64 s[4:5], -1, 0
	s_and_b64 s[4:5], vcc, s[4:5]
	s_cmp_lt_i32 s51, s76
	s_waitcnt vmcnt(44)
	v_cndmask_b32_e64 v34, 0, v34, s[4:5]
	s_cselect_b64 s[4:5], -1, 0
	s_and_b64 s[4:5], vcc, s[4:5]
	s_cmp_lt_i32 s52, s76
	s_waitcnt vmcnt(43)
	v_cndmask_b32_e64 v33, 0, v33, s[4:5]
	s_cselect_b64 s[4:5], -1, 0
	s_and_b64 s[4:5], vcc, s[4:5]
	s_cmp_lt_i32 s53, s76
	s_waitcnt vmcnt(42)
	v_cndmask_b32_e64 v32, 0, v32, s[4:5]
	s_cselect_b64 s[4:5], -1, 0
	s_and_b64 s[4:5], vcc, s[4:5]
	s_cmp_lt_i32 s6, s76
	s_waitcnt vmcnt(41)
	v_cndmask_b32_e64 v31, 0, v31, s[4:5]
	s_cselect_b64 s[4:5], -1, 0
	s_and_b64 s[4:5], vcc, s[4:5]
	s_cmp_lt_i32 s7, s76
	s_waitcnt vmcnt(40)
	v_cndmask_b32_e64 v30, 0, v30, s[4:5]
	s_cselect_b64 s[4:5], -1, 0
	s_and_b64 s[4:5], vcc, s[4:5]
	s_cmp_lt_i32 s8, s76
	s_waitcnt vmcnt(39)
	v_cndmask_b32_e64 v45, 0, v45, s[4:5]
	s_cselect_b64 s[4:5], -1, 0
	s_and_b64 s[4:5], vcc, s[4:5]
	s_cmp_lt_i32 s9, s76
	s_waitcnt vmcnt(38)
	v_cndmask_b32_e64 v44, 0, v44, s[4:5]
	s_cselect_b64 s[4:5], -1, 0
	s_and_b64 s[4:5], vcc, s[4:5]
	s_cmp_lt_i32 s10, s76
	s_waitcnt vmcnt(37)
	v_cndmask_b32_e64 v43, 0, v43, s[4:5]
	s_cselect_b64 s[4:5], -1, 0
	s_and_b64 s[4:5], vcc, s[4:5]
	s_cmp_lt_i32 s11, s76
	s_waitcnt vmcnt(36)
	v_cndmask_b32_e64 v42, 0, v42, s[4:5]
	s_cselect_b64 s[4:5], -1, 0
	s_and_b64 s[4:5], vcc, s[4:5]
	s_cmp_lt_i32 s14, s76
	s_waitcnt vmcnt(35)
	v_cndmask_b32_e64 v41, 0, v41, s[4:5]
	s_cselect_b64 s[4:5], -1, 0
	s_and_b64 s[4:5], vcc, s[4:5]
	s_cmp_lt_i32 s15, s76
	s_waitcnt vmcnt(34)
	v_cndmask_b32_e64 v40, 0, v40, s[4:5]
	s_cselect_b64 s[4:5], -1, 0
	s_and_b64 s[4:5], vcc, s[4:5]
	s_cmp_lt_i32 s16, s76
	s_waitcnt vmcnt(33)
	v_cndmask_b32_e64 v39, 0, v39, s[4:5]
	s_cselect_b64 s[4:5], -1, 0
	s_and_b64 s[4:5], vcc, s[4:5]
	s_cmp_lt_i32 s17, s76
	s_waitcnt vmcnt(32)
	v_cndmask_b32_e64 v38, 0, v38, s[4:5]
	s_cselect_b64 s[4:5], -1, 0
	s_and_b64 s[4:5], vcc, s[4:5]
	s_cmp_lt_i32 s12, s76
	s_waitcnt vmcnt(31)
	v_cndmask_b32_e64 v53, 0, v53, s[4:5]
	s_cselect_b64 s[4:5], -1, 0
	s_and_b64 s[4:5], vcc, s[4:5]
	s_cmp_lt_i32 s13, s76
	s_waitcnt vmcnt(30)
	v_cndmask_b32_e64 v52, 0, v52, s[4:5]
	s_cselect_b64 s[4:5], -1, 0
	s_and_b64 s[4:5], vcc, s[4:5]
	s_cmp_lt_i32 s20, s76
	s_waitcnt vmcnt(29)
	v_cndmask_b32_e64 v51, 0, v51, s[4:5]
	s_cselect_b64 s[4:5], -1, 0
	s_and_b64 s[4:5], vcc, s[4:5]
	s_cmp_lt_i32 s21, s76
	s_waitcnt vmcnt(28)
	v_cndmask_b32_e64 v50, 0, v50, s[4:5]
	s_cselect_b64 s[4:5], -1, 0
	s_and_b64 s[4:5], vcc, s[4:5]
	s_cmp_lt_i32 s24, s76
	s_waitcnt vmcnt(27)
	v_cndmask_b32_e64 v49, 0, v49, s[4:5]
	s_cselect_b64 s[4:5], -1, 0
	s_and_b64 s[4:5], vcc, s[4:5]
	s_cmp_lt_i32 s25, s76
	s_waitcnt vmcnt(26)
	v_cndmask_b32_e64 v48, 0, v48, s[4:5]
	s_cselect_b64 s[4:5], -1, 0
	s_and_b64 s[4:5], vcc, s[4:5]
	s_cmp_lt_i32 s26, s76
	s_waitcnt vmcnt(25)
	v_cndmask_b32_e64 v47, 0, v47, s[4:5]
	s_cselect_b64 s[4:5], -1, 0
	s_and_b64 s[4:5], vcc, s[4:5]
	s_cmp_lt_i32 s27, s76
	s_waitcnt vmcnt(24)
; #define LAS __attribute__((address_space(3)))
; __device__ __forceinline__ void conv_load(const ConvItem& ci, int lane, float (&v)[64]) {
;     ...
;     for (int i = 0; i < 64; ++i) v[i] = (okc && (ci.k0 + i) < ci.Ksrc) ? v[i] : 0.f;
; }
; __device__ __forceinline__ void conv_store(const ConvItem& ci, LAS float* scr, int lane, const float (&v)[64]) {
;     const int c = lane & 7;
;     f32x4 s0 = {1.f, 1.f, 1.f, 1.f}, s1 = s0;
;     if (ci.ks) { const int kb = ci.k0 + 8 * c < ci.Ksrc - 8 ? ci.k0 + 8 * c : ci.Ksrc - 8; s0 = *(const f32x4*)(ci.ks + kb); s1 = *(const f32x4*)(ci.ks + kb + 4); }
; #pragma unroll
;     for (int i = 0; i < 64; ++i) scr[i * 65 + lane] = v[i];
	v_cndmask_b32_e64 v46, 0, v46, s[4:5]
	s_cselect_b64 s[4:5], -1, 0
	s_and_b64 s[4:5], vcc, s[4:5]
	s_cmp_lt_i32 s18, s76
	s_waitcnt vmcnt(23)
	v_cndmask_b32_e64 v61, 0, v61, s[4:5]
	s_cselect_b64 s[4:5], -1, 0
	s_and_b64 s[4:5], vcc, s[4:5]
	s_cmp_lt_i32 s19, s76
	s_waitcnt vmcnt(22)
	v_cndmask_b32_e64 v60, 0, v60, s[4:5]
	s_cselect_b64 s[4:5], -1, 0
	s_and_b64 s[4:5], vcc, s[4:5]
	s_cmp_lt_i32 s28, s76
	s_waitcnt vmcnt(21)
	v_cndmask_b32_e64 v59, 0, v59, s[4:5]
	s_cselect_b64 s[4:5], -1, 0
	s_and_b64 s[4:5], vcc, s[4:5]
	s_cmp_lt_i32 s29, s76
	s_waitcnt vmcnt(20)
	v_cndmask_b32_e64 v58, 0, v58, s[4:5]
	s_cselect_b64 s[4:5], -1, 0
	s_and_b64 s[4:5], vcc, s[4:5]
	s_cmp_lt_i32 s22, s76
	s_waitcnt vmcnt(19)
	v_cndmask_b32_e64 v57, 0, v57, s[4:5]
	s_cselect_b64 s[4:5], -1, 0
	s_and_b64 s[4:5], vcc, s[4:5]
	s_cmp_lt_i32 s23, s76
	s_waitcnt vmcnt(18)
	v_cndmask_b32_e64 v56, 0, v56, s[4:5]
	s_cselect_b64 s[4:5], -1, 0
	s_and_b64 s[4:5], vcc, s[4:5]
	s_cmp_lt_i32 s30, s76
	s_waitcnt vmcnt(17)
	v_cndmask_b32_e64 v55, 0, v55, s[4:5]
	s_cselect_b64 s[4:5], -1, 0
	s_and_b64 s[4:5], vcc, s[4:5]
	s_cmp_lt_i32 s31, s76
	s_waitcnt vmcnt(16)
	v_cndmask_b32_e64 v54, 0, v54, s[4:5]
	s_cselect_b64 s[4:5], -1, 0
	s_and_b64 s[4:5], vcc, s[4:5]
	s_cmp_lt_i32 s36, s76
	s_waitcnt vmcnt(15)
	v_cndmask_b32_e64 v70, 0, v70, s[4:5]
	s_cselect_b64 s[4:5], -1, 0
	s_and_b64 s[4:5], vcc, s[4:5]
	s_cmp_lt_i32 s37, s76
	s_waitcnt vmcnt(14)
	v_cndmask_b32_e64 v69, 0, v69, s[4:5]
	s_cselect_b64 s[4:5], -1, 0
	s_and_b64 s[4:5], vcc, s[4:5]
	s_cmp_lt_i32 s38, s76
	s_waitcnt vmcnt(13)
	v_cndmask_b32_e64 v68, 0, v68, s[4:5]
	s_cselect_b64 s[4:5], -1, 0
	s_and_b64 s[4:5], vcc, s[4:5]
	s_cmp_lt_i32 s39, s76
	s_waitcnt vmcnt(12)
	v_cndmask_b32_e64 v67, 0, v67, s[4:5]
	s_cselect_b64 s[4:5], -1, 0
	s_and_b64 s[4:5], vcc, s[4:5]
	s_cmp_lt_i32 s34, s76
	s_waitcnt vmcnt(11)
	v_cndmask_b32_e64 v66, 0, v66, s[4:5]
	s_cselect_b64 s[4:5], -1, 0
	s_and_b64 s[4:5], vcc, s[4:5]
	s_cmp_lt_i32 s35, s76
	s_waitcnt vmcnt(10)
	v_cndmask_b32_e64 v64, 0, v64, s[4:5]
	s_cselect_b64 s[4:5], -1, 0
	s_and_b64 s[4:5], vcc, s[4:5]
	s_cmp_lt_i32 s42, s76
	s_waitcnt vmcnt(9)
	v_cndmask_b32_e64 v63, 0, v63, s[4:5]
	s_cselect_b64 s[4:5], -1, 0
	s_and_b64 s[4:5], vcc, s[4:5]
	s_cmp_lt_i32 s43, s76
	s_waitcnt vmcnt(8)
	v_cndmask_b32_e64 v62, 0, v62, s[4:5]
	s_cselect_b64 s[4:5], -1, 0
	s_and_b64 s[4:5], vcc, s[4:5]
	s_cmp_lt_i32 s54, s76
	s_waitcnt vmcnt(7)
	v_cndmask_b32_e64 v65, 0, v65, s[4:5]
	s_cselect_b64 s[4:5], -1, 0
	s_and_b64 s[4:5], vcc, s[4:5]
	s_cmp_lt_i32 s55, s76
	s_waitcnt vmcnt(6)
	v_cndmask_b32_e64 v74, 0, v74, s[4:5]
	s_cselect_b64 s[4:5], -1, 0
	s_and_b64 s[4:5], vcc, s[4:5]
	s_cmp_lt_i32 s46, s76
	ds_write2_b32 v12, v21, v20 offset1:65
	ds_write2_b32 v12, v19, v18 offset0:130 offset1:195
	v_add_u32_e32 v18, 0x400, v12
	s_waitcnt vmcnt(5)
	v_cndmask_b32_e64 v73, 0, v73, s[4:5]
	s_cselect_b64 s[4:5], -1, 0
	ds_write2_b32 v18, v17, v16 offset0:4 offset1:69
	ds_write2_b32 v18, v15, v8 offset0:134 offset1:199
	v_add_u32_e32 v8, 0x800, v12
	s_and_b64 s[4:5], vcc, s[4:5]
	ds_write2_b32 v8, v29, v28 offset0:8 offset1:73
	ds_write2_b32 v8, v27, v26 offset0:138 offset1:203
	v_add_u32_e32 v8, 0xc00, v12
	s_cmp_lt_i32 s47, s76
	ds_write2_b32 v8, v25, v24 offset0:12 offset1:77
	ds_write2_b32 v8, v23, v22 offset0:142 offset1:207
	v_add_u32_e32 v8, 0x1000, v12
	s_waitcnt vmcnt(4)
	v_cndmask_b32_e64 v72, 0, v72, s[4:5]
	s_cselect_b64 s[4:5], -1, 0
	ds_write2_b32 v8, v37, v36 offset0:16 offset1:81
	ds_write2_b32 v8, v35, v34 offset0:146 offset1:211
	v_add_u32_e32 v8, 0x1400, v12
	s_and_b64 s[4:5], vcc, s[4:5]
	ds_write2_b32 v8, v33, v32 offset0:20 offset1:85
	ds_write2_b32 v8, v31, v30 offset0:150 offset1:215
	v_add_u32_e32 v8, 0x1800, v12
	s_cmp_lt_i32 s48, s76
	ds_write2_b32 v8, v45, v44 offset0:24 offset1:89
	ds_write2_b32 v8, v43, v42 offset0:154 offset1:219
	v_add_u32_e32 v8, 0x1c00, v12
	s_waitcnt vmcnt(3)
	v_cndmask_b32_e64 v71, 0, v71, s[4:5]
	s_cselect_b64 s[4:5], -1, 0
	ds_write2_b32 v8, v41, v40 offset0:28 offset1:93
	ds_write2_b32 v8, v39, v38 offset0:158 offset1:223
	v_add_u32_e32 v8, 0x2000, v12
	s_and_b64 s[4:5], vcc, s[4:5]
	ds_write2_b32 v8, v53, v52 offset0:32 offset1:97
	ds_write2_b32 v8, v51, v50 offset0:162 offset1:227
	v_add_u32_e32 v8, 0x2400, v12
	s_cmp_lt_i32 s49, s76
	ds_write2_b32 v8, v49, v48 offset0:36 offset1:101
	ds_write2_b32 v8, v47, v46 offset0:166 offset1:231
	v_add_u32_e32 v8, 0x2800, v12
	s_waitcnt vmcnt(2)
	v_cndmask_b32_e64 v77, 0, v77, s[4:5]
	s_cselect_b64 s[4:5], -1, 0
	ds_write2_b32 v8, v61, v60 offset0:40 offset1:105
	ds_write2_b32 v8, v59, v58 offset0:170 offset1:235
	v_add_u32_e32 v8, 0x2c00, v12
	s_and_b64 s[4:5], vcc, s[4:5]
	ds_write2_b32 v8, v57, v56 offset0:44 offset1:109
	ds_write2_b32 v8, v55, v54 offset0:174 offset1:239
	v_add_u32_e32 v8, 0x3000, v12
	s_cmp_lt_i32 s44, s76
	ds_write2_b32 v8, v70, v69 offset0:48 offset1:113
	ds_write2_b32 v8, v68, v67 offset0:178 offset1:243
	v_add_u32_e32 v8, 0x3400, v12
	s_waitcnt vmcnt(1)
	v_cndmask_b32_e64 v76, 0, v76, s[4:5]
	s_cselect_b64 s[4:5], -1, 0
	ds_write2_b32 v8, v66, v64 offset0:52 offset1:117
	ds_write2_b32 v8, v63, v62 offset0:182 offset1:247
	v_add_u32_e32 v8, 0x3800, v12
	s_and_b64 vcc, vcc, s[4:5]
	ds_write2_b32 v8, v65, v74 offset0:56 offset1:121
	ds_write2_b32 v8, v73, v72 offset0:186 offset1:251
	v_add_u32_e32 v8, 0x3c00, v12
	s_waitcnt vmcnt(0)
	v_cndmask_b32_e32 v75, 0, v75, vcc
	ds_write2_b32 v8, v71, v77 offset0:60 offset1:125
	ds_write2_b32 v8, v76, v75 offset0:190 offset1:255
	s_waitcnt lgkmcnt(0)
; __device__ __forceinline__ unsigned cvt_pk_bf16(float lo, float hi) { unsigned r; asm volatile("v_cvt_pk_bf16_f32 %0, %1, %2" : "=v"(r) : "v"(lo), "v"(hi)); return r; }
; #define LAS __attribute__((address_space(3)))
; __device__ __forceinline__ void conv_store(const ConvItem& ci, LAS float* scr, int lane, const float (&v)[64]) {
;     ...
;     for (int j = 0; j < 8; ++j) { const int n = (lane >> 3) + 8 * j; const LAS float* s = scr + (8 * c) * 65 + n;
;         v4u o; o.x = cvt_pk_bf16(s[0 * 65] * s0[0], s[1 * 65] * s0[1]); o.y = cvt_pk_bf16(s[2 * 65] * s0[2], s[3 * 65] * s0[3]); o.z = cvt_pk_bf16(s[4 * 65] * s1[0], s[5 * 65] * s1[1]); o.w = cvt_pk_bf16(s[6 * 65] * s1[2], s[7 * 65] * s1[3]);
;         *(v4u*)(ci.dst + (size_t)(ci.drow0 + n) * ci.ldd + ci.k0 + 8 * c) = o; }
	v_add_u32_e32 v192, 0x400, v14
	ds_read2_b32 v[128:129], v14 offset1:65
	ds_read2_b32 v[130:131], v14 offset0:130 offset1:195
	ds_read2_b32 v[132:133], v192 offset0:4 offset1:69
	ds_read2_b32 v[134:135], v192 offset0:134 offset1:199
	ds_read2_b32 v[136:137], v14 offset0:8 offset1:73
	ds_read2_b32 v[138:139], v14 offset0:138 offset1:203
	ds_read2_b32 v[140:141], v192 offset0:12 offset1:77
	ds_read2_b32 v[142:143], v192 offset0:142 offset1:207
	ds_read2_b32 v[144:145], v14 offset0:16 offset1:81
	ds_read2_b32 v[146:147], v14 offset0:146 offset1:211
	ds_read2_b32 v[148:149], v192 offset0:20 offset1:85
	ds_read2_b32 v[150:151], v192 offset0:150 offset1:215
	ds_read2_b32 v[152:153], v14 offset0:24 offset1:89
	ds_read2_b32 v[154:155], v14 offset0:154 offset1:219
	ds_read2_b32 v[156:157], v192 offset0:28 offset1:93
	ds_read2_b32 v[158:159], v192 offset0:158 offset1:223
	ds_read2_b32 v[160:161], v14 offset0:32 offset1:97
	ds_read2_b32 v[162:163], v14 offset0:162 offset1:227
	ds_read2_b32 v[164:165], v192 offset0:36 offset1:101
	ds_read2_b32 v[166:167], v192 offset0:166 offset1:231
	ds_read2_b32 v[168:169], v14 offset0:40 offset1:105
	ds_read2_b32 v[170:171], v14 offset0:170 offset1:235
	ds_read2_b32 v[172:173], v192 offset0:44 offset1:109
	ds_read2_b32 v[174:175], v192 offset0:174 offset1:239
	ds_read2_b32 v[176:177], v14 offset0:48 offset1:113
	ds_read2_b32 v[178:179], v14 offset0:178 offset1:243
	ds_read2_b32 v[180:181], v192 offset0:52 offset1:117
	ds_read2_b32 v[182:183], v192 offset0:182 offset1:247
	ds_read2_b32 v[184:185], v14 offset0:56 offset1:121
	ds_read2_b32 v[186:187], v14 offset0:186 offset1:251
	ds_read2_b32 v[188:189], v192 offset0:60 offset1:125
	ds_read2_b32 v[190:191], v192 offset0:190 offset1:255
	s_waitcnt lgkmcnt(0)
	v_add_u32_e32 v24, s59, v13
	v_mul_lo_u32 v22, s57, v24
	s_ashr_i32 s59, s58, 31
	v_readlane_b32 s76, v254, 31
	s_waitcnt lgkmcnt(0)
	v_mul_f32_e32 v8, v4, v128
	v_mul_f32_e32 v15, v5, v129
	v_cvt_pk_bf16_f32 v16, v8, v15
	s_add_i32 s3, s3, s33
	s_add_i32 s66, s66, s67
	s_add_i32 s68, s68, s69
	s_add_i32 s70, s70, s71
	s_waitcnt lgkmcnt(0)
	v_mul_f32_e32 v15, v7, v131
	v_mul_f32_e32 v8, v6, v130
	v_cvt_pk_bf16_f32 v17, v8, v15
	v_add_u32_e32 v15, 0x400, v14
	s_add_i32 s72, s72, s73
	s_add_i32 s74, s74, s75
	v_readlane_b32 s78, v254, 33
	v_readlane_b32 s79, v254, 34
	s_waitcnt lgkmcnt(0)
	v_mul_f32_e32 v8, v0, v132
	v_mul_f32_e32 v18, v1, v133
	v_cvt_pk_bf16_f32 v18, v8, v18
	v_readlane_b32 s80, v255, 21
	v_readlane_b32 s77, v254, 32
	s_movk_i32 s78, 0x1580
	v_readlane_b32 s82, v255, 23
	s_waitcnt lgkmcnt(0)
	v_mul_f32_e32 v8, v2, v134
	v_mul_f32_e32 v19, v3, v135
	v_cvt_pk_bf16_f32 v19, v8, v19
	v_ashrrev_i32_e32 v8, 31, v24
	v_mul_lo_u32 v8, s56, v8
	v_mad_u64_u32 v[20:21], s[4:5], s56, v24, 0
	v_add3_u32 v21, v21, v8, v22
	v_lshl_add_u64 v[20:21], v[20:21], 1, s[60:61]
	s_lshl_b64 s[4:5], s[58:59], 1
	v_lshl_add_u64 v[20:21], v[20:21], 0, s[4:5]
	v_lshlrev_b32_e32 v8, 1, v10
	v_lshl_add_u64 v[20:21], v[20:21], 0, v[8:9]
	global_store_dwordx4 v[20:21], v[16:19], off sc1 nt
	s_cmpk_lt_i32 s3, 26496
	v_readlane_b32 s83, v255, 24
	s_waitcnt lgkmcnt(0)
	v_mul_f32_e32 v16, v4, v136
	v_mul_f32_e32 v17, v5, v137
	v_cvt_pk_bf16_f32 v16, v16, v17
	s_mov_b32 s79, 0x3f22f983
	s_mov_b32 s85, 0xbfc90fda
	s_brev_b32 s86, 1
	s_movk_i32 s87, 0x1f8
	s_waitcnt lgkmcnt(0)
	v_mul_f32_e32 v17, v6, v138
	v_mul_f32_e32 v18, v7, v139
	v_cvt_pk_bf16_f32 v17, v17, v18
	s_mov_b64 s[88:89], 0x80
	s_mov_b64 s[92:93], 0x4000
	s_mov_b64 s[94:95], 0x4800
	v_readlane_b32 s81, v255, 22
	s_waitcnt lgkmcnt(0)
	v_mul_f32_e32 v18, v0, v140
	v_mul_f32_e32 v19, v1, v141
	v_cvt_pk_bf16_f32 v18, v18, v19
	s_waitcnt lgkmcnt(0)
	v_mul_f32_e32 v19, v2, v142
	v_mul_f32_e32 v20, v3, v143
	v_cvt_pk_bf16_f32 v19, v19, v20
	v_add_u32_e32 v20, 8, v24
	v_ashrrev_i32_e32 v21, 31, v20
	v_mul_lo_u32 v22, s56, v21
	v_mul_lo_u32 v23, s57, v20
	v_mad_u64_u32 v[20:21], s[6:7], s56, v20, 0
	v_add3_u32 v21, v21, v22, v23
	v_lshl_add_u64 v[20:21], v[20:21], 1, s[60:61]
	v_lshl_add_u64 v[20:21], v[20:21], 0, s[4:5]
	v_lshl_add_u64 v[20:21], v[20:21], 0, v[8:9]
	global_store_dwordx4 v[20:21], v[16:19], off sc1 nt
	s_waitcnt lgkmcnt(0)
	s_nop 0
	v_mul_f32_e32 v16, v4, v144
	v_mul_f32_e32 v17, v5, v145
	v_cvt_pk_bf16_f32 v16, v16, v17
	s_waitcnt lgkmcnt(0)
	v_mul_f32_e32 v17, v6, v146
	v_mul_f32_e32 v18, v7, v147
	v_cvt_pk_bf16_f32 v17, v17, v18
	s_waitcnt lgkmcnt(0)
	v_mul_f32_e32 v18, v0, v148
	v_mul_f32_e32 v19, v1, v149
	v_cvt_pk_bf16_f32 v18, v18, v19
	s_waitcnt lgkmcnt(0)
; __device__ __forceinline__ unsigned cvt_pk_bf16(float lo, float hi) { unsigned r; asm volatile("v_cvt_pk_bf16_f32 %0, %1, %2" : "=v"(r) : "v"(lo), "v"(hi)); return r; }
; #define LAS __attribute__((address_space(3)))
; __device__ __forceinline__ void conv_store(const ConvItem& ci, LAS float* scr, int lane, const float (&v)[64]) {
;     ...
;     for (int j = 0; j < 8; ++j) { const int n = (lane >> 3) + 8 * j; const LAS float* s = scr + (8 * c) * 65 + n;
;         v4u o; o.x = cvt_pk_bf16(s[0 * 65] * s0[0], s[1 * 65] * s0[1]); o.y = cvt_pk_bf16(s[2 * 65] * s0[2], s[3 * 65] * s0[3]); o.z = cvt_pk_bf16(s[4 * 65] * s1[0], s[5 * 65] * s1[1]); o.w = cvt_pk_bf16(s[6 * 65] * s1[2], s[7 * 65] * s1[3]);
;         *(v4u*)(ci.dst + (size_t)(ci.drow0 + n) * ci.ldd + ci.k0 + 8 * c) = o; }
	v_mul_f32_e32 v19, v2, v150
	v_mul_f32_e32 v20, v3, v151
	v_cvt_pk_bf16_f32 v19, v19, v20
	v_add_u32_e32 v20, 16, v24
	v_ashrrev_i32_e32 v21, 31, v20
	v_mul_lo_u32 v22, s56, v21
	v_mul_lo_u32 v23, s57, v20
	v_mad_u64_u32 v[20:21], s[6:7], s56, v20, 0
	v_add3_u32 v21, v21, v22, v23
	v_lshl_add_u64 v[20:21], v[20:21], 1, s[60:61]
	v_lshl_add_u64 v[20:21], v[20:21], 0, s[4:5]
	v_lshl_add_u64 v[20:21], v[20:21], 0, v[8:9]
	global_store_dwordx4 v[20:21], v[16:19], off sc1 nt
	s_waitcnt lgkmcnt(0)
	s_nop 0
	v_mul_f32_e32 v16, v4, v152
	v_mul_f32_e32 v17, v5, v153
	v_cvt_pk_bf16_f32 v16, v16, v17
	s_waitcnt lgkmcnt(0)
	v_mul_f32_e32 v17, v6, v154
	v_mul_f32_e32 v18, v7, v155
	v_cvt_pk_bf16_f32 v17, v17, v18
	s_waitcnt lgkmcnt(0)
	v_mul_f32_e32 v18, v0, v156
	v_mul_f32_e32 v19, v1, v157
	v_cvt_pk_bf16_f32 v18, v18, v19
	s_waitcnt lgkmcnt(0)
	v_mul_f32_e32 v19, v2, v158
	v_mul_f32_e32 v20, v3, v159
	v_cvt_pk_bf16_f32 v19, v19, v20
	v_add_u32_e32 v20, 24, v24
	v_ashrrev_i32_e32 v21, 31, v20
	v_mul_lo_u32 v22, s56, v21
	v_mul_lo_u32 v23, s57, v20
	v_mad_u64_u32 v[20:21], s[6:7], s56, v20, 0
	v_add3_u32 v21, v21, v22, v23
	v_lshl_add_u64 v[20:21], v[20:21], 1, s[60:61]
	v_lshl_add_u64 v[20:21], v[20:21], 0, s[4:5]
	v_lshl_add_u64 v[20:21], v[20:21], 0, v[8:9]
	global_store_dwordx4 v[20:21], v[16:19], off sc1 nt
	s_waitcnt lgkmcnt(0)
	s_nop 0
	v_mul_f32_e32 v16, v4, v160
	v_mul_f32_e32 v17, v5, v161
	v_cvt_pk_bf16_f32 v16, v16, v17
	s_waitcnt lgkmcnt(0)
	v_mul_f32_e32 v17, v6, v162
	v_mul_f32_e32 v18, v7, v163
	v_cvt_pk_bf16_f32 v17, v17, v18
	s_waitcnt lgkmcnt(0)
	v_mul_f32_e32 v18, v0, v164
	v_mul_f32_e32 v19, v1, v165
	v_cvt_pk_bf16_f32 v18, v18, v19
	s_waitcnt lgkmcnt(0)
	v_mul_f32_e32 v19, v2, v166
	v_mul_f32_e32 v20, v3, v167
	v_cvt_pk_bf16_f32 v19, v19, v20
	v_add_u32_e32 v20, 32, v24
	v_ashrrev_i32_e32 v21, 31, v20
	v_mul_lo_u32 v22, s56, v21
	v_mul_lo_u32 v23, s57, v20
	v_mad_u64_u32 v[20:21], s[6:7], s56, v20, 0
	v_add3_u32 v21, v21, v22, v23
	v_lshl_add_u64 v[20:21], v[20:21], 1, s[60:61]
	v_lshl_add_u64 v[20:21], v[20:21], 0, s[4:5]
	v_lshl_add_u64 v[20:21], v[20:21], 0, v[8:9]
	global_store_dwordx4 v[20:21], v[16:19], off sc1 nt
	s_waitcnt lgkmcnt(0)
	s_nop 0
	v_mul_f32_e32 v16, v4, v168
	v_mul_f32_e32 v17, v5, v169
	v_cvt_pk_bf16_f32 v16, v16, v17
	s_waitcnt lgkmcnt(0)
	v_mul_f32_e32 v17, v6, v170
	v_mul_f32_e32 v18, v7, v171
	v_cvt_pk_bf16_f32 v17, v17, v18
	s_waitcnt lgkmcnt(0)
	v_mul_f32_e32 v18, v0, v172
	v_mul_f32_e32 v19, v1, v173
	v_cvt_pk_bf16_f32 v18, v18, v19
	s_waitcnt lgkmcnt(0)
	v_mul_f32_e32 v19, v2, v174
	v_mul_f32_e32 v20, v3, v175
	v_cvt_pk_bf16_f32 v19, v19, v20
	v_add_u32_e32 v20, 40, v24
	v_ashrrev_i32_e32 v21, 31, v20
	v_mul_lo_u32 v22, s56, v21
	v_mul_lo_u32 v23, s57, v20
	v_mad_u64_u32 v[20:21], s[6:7], s56, v20, 0
	v_add3_u32 v21, v21, v22, v23
	v_lshl_add_u64 v[20:21], v[20:21], 1, s[60:61]
	v_lshl_add_u64 v[20:21], v[20:21], 0, s[4:5]
	v_lshl_add_u64 v[20:21], v[20:21], 0, v[8:9]
	global_store_dwordx4 v[20:21], v[16:19], off sc1 nt
	s_waitcnt lgkmcnt(0)
	s_nop 0
	v_mul_f32_e32 v16, v4, v176
	v_mul_f32_e32 v17, v5, v177
	v_cvt_pk_bf16_f32 v16, v16, v17
	s_waitcnt lgkmcnt(0)
	v_mul_f32_e32 v17, v6, v178
	v_mul_f32_e32 v18, v7, v179
	v_cvt_pk_bf16_f32 v17, v17, v18
	s_waitcnt lgkmcnt(0)
	v_mul_f32_e32 v18, v0, v180
	v_mul_f32_e32 v19, v1, v181
	v_cvt_pk_bf16_f32 v18, v18, v19
	s_waitcnt lgkmcnt(0)
	v_mul_f32_e32 v19, v2, v182
	v_mul_f32_e32 v20, v3, v183
	v_cvt_pk_bf16_f32 v19, v19, v20
	v_add_u32_e32 v20, 48, v24
	v_ashrrev_i32_e32 v21, 31, v20
	v_mul_lo_u32 v22, s56, v21
	v_mul_lo_u32 v23, s57, v20
	v_mad_u64_u32 v[20:21], s[6:7], s56, v20, 0
	v_add3_u32 v21, v21, v22, v23
	v_lshl_add_u64 v[20:21], v[20:21], 1, s[60:61]
	v_lshl_add_u64 v[20:21], v[20:21], 0, s[4:5]
	v_lshl_add_u64 v[20:21], v[20:21], 0, v[8:9]
	global_store_dwordx4 v[20:21], v[16:19], off sc1 nt
	s_waitcnt lgkmcnt(0)
	v_mul_f32_e32 v4, v4, v184
	v_mul_f32_e32 v5, v5, v185
	v_cvt_pk_bf16_f32 v4, v4, v5
	s_waitcnt lgkmcnt(0)
	v_mul_f32_e32 v5, v6, v186
	v_mul_f32_e32 v6, v7, v187
	v_cvt_pk_bf16_f32 v5, v5, v6
	s_waitcnt lgkmcnt(0)
	v_mul_f32_e32 v0, v0, v188
	v_mul_f32_e32 v1, v1, v189
	v_cvt_pk_bf16_f32 v6, v0, v1
	s_waitcnt lgkmcnt(0)
	v_mul_f32_e32 v0, v2, v190
	v_mul_f32_e32 v1, v3, v191
	v_cvt_pk_bf16_f32 v7, v0, v1
	v_add_u32_e32 v0, 56, v24
	v_ashrrev_i32_e32 v1, 31, v0
	v_mul_lo_u32 v2, s56, v1
	v_mul_lo_u32 v3, s57, v0
	v_mad_u64_u32 v[0:1], s[6:7], s56, v0, 0
	v_add3_u32 v1, v1, v2, v3
	v_lshl_add_u64 v[0:1], v[0:1], 1, s[60:61]
	v_lshl_add_u64 v[0:1], v[0:1], 0, s[4:5]
	v_lshl_add_u64 v[0:1], v[0:1], 0, v[8:9]
	global_store_dwordx4 v[0:1], v[4:7], off sc1 nt
	s_waitcnt lgkmcnt(0)
	s_cbranch_scc0 .Lcvp11_ret

; __device__ __forceinline__ void conv_load(const ConvItem& ci, int lane, float (&v)[64]) {
;     ...
;     for (int i = 0; i < 64; ++i) { const int k = ci.k0 + i, kk = k < kmax ? k : kmax; v[i] = __builtin_nontemporal_load(base + (size_t)kk * ci.ldw); }
; #pragma unroll
;     for (int i = 0; i < 64; ++i) v[i] = (okc && (ci.k0 + i) < ci.Ksrc) ? v[i] : 0.f;
.Lcvp30_30:
	s_cmp_lt_i32 s58, s76
	s_cselect_b64 s[4:5], -1, 0
	s_and_b64 s[4:5], vcc, s[4:5]
	s_cmp_lt_i32 s64, s76
	s_waitcnt vmcnt(62)
	v_cndmask_b32_e64 v21, 0, v21, s[4:5]
	s_cselect_b64 s[4:5], -1, 0
	s_and_b64 s[4:5], vcc, s[4:5]
	s_cmp_lt_i32 s65, s76
	v_cndmask_b32_e64 v20, 0, v20, s[4:5]
	s_cselect_b64 s[4:5], -1, 0
	s_and_b64 s[4:5], vcc, s[4:5]
	s_cmp_lt_i32 s78, s76
	s_waitcnt vmcnt(61)
	v_cndmask_b32_e64 v19, 0, v19, s[4:5]
	s_cselect_b64 s[4:5], -1, 0
	s_and_b64 s[4:5], vcc, s[4:5]
	s_cmp_lt_i32 s79, s76
	s_waitcnt vmcnt(60)
	v_cndmask_b32_e64 v18, 0, v18, s[4:5]
	s_cselect_b64 s[4:5], -1, 0
	s_and_b64 s[4:5], vcc, s[4:5]
	s_cmp_lt_i32 s80, s76
	s_waitcnt vmcnt(59)
	v_cndmask_b32_e64 v17, 0, v17, s[4:5]
	s_cselect_b64 s[4:5], -1, 0
	s_and_b64 s[4:5], vcc, s[4:5]
	s_cmp_lt_i32 s81, s76
	s_waitcnt vmcnt(58)
	v_cndmask_b32_e64 v16, 0, v16, s[4:5]
	s_cselect_b64 s[4:5], -1, 0
	s_and_b64 s[4:5], vcc, s[4:5]
	s_cmp_lt_i32 s82, s76
	s_waitcnt vmcnt(57)
	v_cndmask_b32_e64 v15, 0, v15, s[4:5]
	s_cselect_b64 s[4:5], -1, 0
	s_and_b64 s[4:5], vcc, s[4:5]
	s_cmp_lt_i32 s83, s76
	s_waitcnt vmcnt(56)
	v_cndmask_b32_e64 v8, 0, v8, s[4:5]
	s_cselect_b64 s[4:5], -1, 0
	s_and_b64 s[4:5], vcc, s[4:5]
	s_cmp_lt_i32 s85, s76
	s_waitcnt vmcnt(55)
	v_cndmask_b32_e64 v29, 0, v29, s[4:5]
	s_cselect_b64 s[4:5], -1, 0
	s_and_b64 s[4:5], vcc, s[4:5]
	s_cmp_lt_i32 s86, s76
	s_waitcnt vmcnt(54)
	v_cndmask_b32_e64 v28, 0, v28, s[4:5]
	s_cselect_b64 s[4:5], -1, 0
	s_and_b64 s[4:5], vcc, s[4:5]
	s_cmp_lt_i32 s87, s76
	s_waitcnt vmcnt(53)
	v_cndmask_b32_e64 v27, 0, v27, s[4:5]
	s_cselect_b64 s[4:5], -1, 0
	s_and_b64 s[4:5], vcc, s[4:5]
	s_cmp_lt_i32 s88, s76
	s_waitcnt vmcnt(52)
	v_cndmask_b32_e64 v26, 0, v26, s[4:5]
	s_cselect_b64 s[4:5], -1, 0
	s_and_b64 s[4:5], vcc, s[4:5]
	s_cmp_lt_i32 s89, s76
	s_waitcnt vmcnt(51)
	v_cndmask_b32_e64 v25, 0, v25, s[4:5]
	s_cselect_b64 s[4:5], -1, 0
	s_and_b64 s[4:5], vcc, s[4:5]
	s_cmp_lt_i32 s90, s76
	s_waitcnt vmcnt(50)
	v_cndmask_b32_e64 v24, 0, v24, s[4:5]
	s_cselect_b64 s[4:5], -1, 0
	s_and_b64 s[4:5], vcc, s[4:5]
	s_cmp_lt_i32 s92, s76
	s_waitcnt vmcnt(49)
	v_cndmask_b32_e64 v23, 0, v23, s[4:5]
	s_cselect_b64 s[4:5], -1, 0
	s_and_b64 s[4:5], vcc, s[4:5]
	s_cmp_lt_i32 s93, s76
	s_waitcnt vmcnt(48)
	v_cndmask_b32_e64 v22, 0, v22, s[4:5]
	s_cselect_b64 s[4:5], -1, 0
	s_and_b64 s[4:5], vcc, s[4:5]
	s_cmp_lt_i32 s94, s76
	s_waitcnt vmcnt(47)
	v_cndmask_b32_e64 v37, 0, v37, s[4:5]
	s_cselect_b64 s[4:5], -1, 0
	s_and_b64 s[4:5], vcc, s[4:5]
	s_cmp_lt_i32 s95, s76
	s_waitcnt vmcnt(46)
	v_cndmask_b32_e64 v36, 0, v36, s[4:5]
	s_cselect_b64 s[4:5], -1, 0
	s_and_b64 s[4:5], vcc, s[4:5]
	s_cmp_lt_i32 s50, s76
	s_waitcnt vmcnt(45)
	v_cndmask_b32_e64 v35, 0, v35, s[4:5]
	s_cselect_b64 s[4:5], -1, 0
	s_and_b64 s[4:5], vcc, s[4:5]
	s_cmp_lt_i32 s51, s76
	s_waitcnt vmcnt(44)
	v_cndmask_b32_e64 v34, 0, v34, s[4:5]
	s_cselect_b64 s[4:5], -1, 0
	s_and_b64 s[4:5], vcc, s[4:5]
	s_cmp_lt_i32 s52, s76
	s_waitcnt vmcnt(43)
	v_cndmask_b32_e64 v33, 0, v33, s[4:5]
	s_cselect_b64 s[4:5], -1, 0
	s_and_b64 s[4:5], vcc, s[4:5]
	s_cmp_lt_i32 s53, s76
	s_waitcnt vmcnt(42)
	v_cndmask_b32_e64 v32, 0, v32, s[4:5]
	s_cselect_b64 s[4:5], -1, 0
	s_and_b64 s[4:5], vcc, s[4:5]
	s_cmp_lt_i32 s6, s76
	s_waitcnt vmcnt(41)
	v_cndmask_b32_e64 v31, 0, v31, s[4:5]
	s_cselect_b64 s[4:5], -1, 0
	s_and_b64 s[4:5], vcc, s[4:5]
	s_cmp_lt_i32 s7, s76
	s_waitcnt vmcnt(40)
	v_cndmask_b32_e64 v30, 0, v30, s[4:5]
	s_cselect_b64 s[4:5], -1, 0
	s_and_b64 s[4:5], vcc, s[4:5]
	s_cmp_lt_i32 s8, s76
	s_waitcnt vmcnt(39)
	v_cndmask_b32_e64 v45, 0, v45, s[4:5]
	s_cselect_b64 s[4:5], -1, 0
	s_and_b64 s[4:5], vcc, s[4:5]
	s_cmp_lt_i32 s9, s76
	s_waitcnt vmcnt(38)
	v_cndmask_b32_e64 v44, 0, v44, s[4:5]
	s_cselect_b64 s[4:5], -1, 0
	s_and_b64 s[4:5], vcc, s[4:5]
	s_cmp_lt_i32 s10, s76
	s_waitcnt vmcnt(37)
	v_cndmask_b32_e64 v43, 0, v43, s[4:5]
	s_cselect_b64 s[4:5], -1, 0
	s_and_b64 s[4:5], vcc, s[4:5]
	s_cmp_lt_i32 s11, s76
	s_waitcnt vmcnt(36)
	v_cndmask_b32_e64 v42, 0, v42, s[4:5]
	s_cselect_b64 s[4:5], -1, 0
	s_and_b64 s[4:5], vcc, s[4:5]
	s_cmp_lt_i32 s14, s76
	s_waitcnt vmcnt(35)
	v_cndmask_b32_e64 v41, 0, v41, s[4:5]
	s_cselect_b64 s[4:5], -1, 0
	s_and_b64 s[4:5], vcc, s[4:5]
	s_cmp_lt_i32 s15, s76
	s_waitcnt vmcnt(34)
	v_cndmask_b32_e64 v40, 0, v40, s[4:5]
	s_cselect_b64 s[4:5], -1, 0
	s_and_b64 s[4:5], vcc, s[4:5]
	s_cmp_lt_i32 s16, s76
	s_waitcnt vmcnt(33)
	v_cndmask_b32_e64 v39, 0, v39, s[4:5]
	s_cselect_b64 s[4:5], -1, 0
	s_and_b64 s[4:5], vcc, s[4:5]
	s_cmp_lt_i32 s17, s76
	s_waitcnt vmcnt(32)
	v_cndmask_b32_e64 v38, 0, v38, s[4:5]
	s_cselect_b64 s[4:5], -1, 0
	s_and_b64 s[4:5], vcc, s[4:5]
	s_cmp_lt_i32 s12, s76
	s_waitcnt vmcnt(31)
	v_cndmask_b32_e64 v53, 0, v53, s[4:5]
	s_cselect_b64 s[4:5], -1, 0
	s_and_b64 s[4:5], vcc, s[4:5]
	s_cmp_lt_i32 s13, s76
	s_waitcnt vmcnt(30)
	v_cndmask_b32_e64 v52, 0, v52, s[4:5]
	s_cselect_b64 s[4:5], -1, 0
	s_and_b64 s[4:5], vcc, s[4:5]
	s_cmp_lt_i32 s20, s76
	s_waitcnt vmcnt(29)
	v_cndmask_b32_e64 v51, 0, v51, s[4:5]
	s_cselect_b64 s[4:5], -1, 0
	s_and_b64 s[4:5], vcc, s[4:5]
	s_cmp_lt_i32 s21, s76
	s_waitcnt vmcnt(28)
	v_cndmask_b32_e64 v50, 0, v50, s[4:5]
	s_cselect_b64 s[4:5], -1, 0
	s_and_b64 s[4:5], vcc, s[4:5]
	s_cmp_lt_i32 s24, s76
	s_waitcnt vmcnt(27)
	v_cndmask_b32_e64 v49, 0, v49, s[4:5]
	s_cselect_b64 s[4:5], -1, 0
	s_and_b64 s[4:5], vcc, s[4:5]
	s_cmp_lt_i32 s25, s76
	s_waitcnt vmcnt(26)
	v_cndmask_b32_e64 v48, 0, v48, s[4:5]
	s_cselect_b64 s[4:5], -1, 0
	s_and_b64 s[4:5], vcc, s[4:5]
	s_cmp_lt_i32 s26, s76
	s_waitcnt vmcnt(25)
	v_cndmask_b32_e64 v47, 0, v47, s[4:5]
	s_cselect_b64 s[4:5], -1, 0
	s_and_b64 s[4:5], vcc, s[4:5]
	s_cmp_lt_i32 s27, s76
	s_waitcnt vmcnt(24)
; #define LAS __attribute__((address_space(3)))
; __device__ __forceinline__ void conv_load(const ConvItem& ci, int lane, float (&v)[64]) {
;     ...
;     for (int i = 0; i < 64; ++i) v[i] = (okc && (ci.k0 + i) < ci.Ksrc) ? v[i] : 0.f;
; }
; __device__ __forceinline__ void conv_store(const ConvItem& ci, LAS float* scr, int lane, const float (&v)[64]) {
;     const int c = lane & 7;
;     f32x4 s0 = {1.f, 1.f, 1.f, 1.f}, s1 = s0;
;     if (ci.ks) { const int kb = ci.k0 + 8 * c < ci.Ksrc - 8 ? ci.k0 + 8 * c : ci.Ksrc - 8; s0 = *(const f32x4*)(ci.ks + kb); s1 = *(const f32x4*)(ci.ks + kb + 4); }
; #pragma unroll
;     for (int i = 0; i < 64; ++i) scr[i * 65 + lane] = v[i];
	v_cndmask_b32_e64 v46, 0, v46, s[4:5]
	s_cselect_b64 s[4:5], -1, 0
	s_and_b64 s[4:5], vcc, s[4:5]
	s_cmp_lt_i32 s18, s76
	s_waitcnt vmcnt(23)
	v_cndmask_b32_e64 v61, 0, v61, s[4:5]
	s_cselect_b64 s[4:5], -1, 0
	s_and_b64 s[4:5], vcc, s[4:5]
	s_cmp_lt_i32 s19, s76
	s_waitcnt vmcnt(22)
	v_cndmask_b32_e64 v60, 0, v60, s[4:5]
	s_cselect_b64 s[4:5], -1, 0
	s_and_b64 s[4:5], vcc, s[4:5]
	s_cmp_lt_i32 s28, s76
	s_waitcnt vmcnt(21)
	v_cndmask_b32_e64 v59, 0, v59, s[4:5]
	s_cselect_b64 s[4:5], -1, 0
	s_and_b64 s[4:5], vcc, s[4:5]
	s_cmp_lt_i32 s29, s76
	s_waitcnt vmcnt(20)
	v_cndmask_b32_e64 v58, 0, v58, s[4:5]
	s_cselect_b64 s[4:5], -1, 0
	s_and_b64 s[4:5], vcc, s[4:5]
	s_cmp_lt_i32 s22, s76
	s_waitcnt vmcnt(19)
	v_cndmask_b32_e64 v57, 0, v57, s[4:5]
	s_cselect_b64 s[4:5], -1, 0
	s_and_b64 s[4:5], vcc, s[4:5]
	s_cmp_lt_i32 s23, s76
	s_waitcnt vmcnt(18)
	v_cndmask_b32_e64 v56, 0, v56, s[4:5]
	s_cselect_b64 s[4:5], -1, 0
	s_and_b64 s[4:5], vcc, s[4:5]
	s_cmp_lt_i32 s30, s76
	s_waitcnt vmcnt(17)
	v_cndmask_b32_e64 v55, 0, v55, s[4:5]
	s_cselect_b64 s[4:5], -1, 0
	s_and_b64 s[4:5], vcc, s[4:5]
	s_cmp_lt_i32 s31, s76
	s_waitcnt vmcnt(16)
	v_cndmask_b32_e64 v54, 0, v54, s[4:5]
	s_cselect_b64 s[4:5], -1, 0
	s_and_b64 s[4:5], vcc, s[4:5]
	s_cmp_lt_i32 s36, s76
	s_waitcnt vmcnt(15)
	v_cndmask_b32_e64 v70, 0, v70, s[4:5]
	s_cselect_b64 s[4:5], -1, 0
	s_and_b64 s[4:5], vcc, s[4:5]
	s_cmp_lt_i32 s37, s76
	s_waitcnt vmcnt(14)
	v_cndmask_b32_e64 v69, 0, v69, s[4:5]
	s_cselect_b64 s[4:5], -1, 0
	s_and_b64 s[4:5], vcc, s[4:5]
	s_cmp_lt_i32 s38, s76
	s_waitcnt vmcnt(13)
	v_cndmask_b32_e64 v68, 0, v68, s[4:5]
	s_cselect_b64 s[4:5], -1, 0
	s_and_b64 s[4:5], vcc, s[4:5]
	s_cmp_lt_i32 s39, s76
	s_waitcnt vmcnt(12)
	v_cndmask_b32_e64 v67, 0, v67, s[4:5]
	s_cselect_b64 s[4:5], -1, 0
	s_and_b64 s[4:5], vcc, s[4:5]
	s_cmp_lt_i32 s34, s76
	s_waitcnt vmcnt(11)
	v_cndmask_b32_e64 v66, 0, v66, s[4:5]
	s_cselect_b64 s[4:5], -1, 0
	s_and_b64 s[4:5], vcc, s[4:5]
	s_cmp_lt_i32 s35, s76
	s_waitcnt vmcnt(10)
	v_cndmask_b32_e64 v64, 0, v64, s[4:5]
	s_cselect_b64 s[4:5], -1, 0
	s_and_b64 s[4:5], vcc, s[4:5]
	s_cmp_lt_i32 s42, s76
	s_waitcnt vmcnt(9)
	v_cndmask_b32_e64 v63, 0, v63, s[4:5]
	s_cselect_b64 s[4:5], -1, 0
	s_and_b64 s[4:5], vcc, s[4:5]
	s_cmp_lt_i32 s43, s76
	s_waitcnt vmcnt(8)
	v_cndmask_b32_e64 v62, 0, v62, s[4:5]
	s_cselect_b64 s[4:5], -1, 0
	s_and_b64 s[4:5], vcc, s[4:5]
	s_cmp_lt_i32 s54, s76
	s_waitcnt vmcnt(7)
	v_cndmask_b32_e64 v65, 0, v65, s[4:5]
	s_cselect_b64 s[4:5], -1, 0
	s_and_b64 s[4:5], vcc, s[4:5]
	s_cmp_lt_i32 s55, s76
	s_waitcnt vmcnt(6)
	v_cndmask_b32_e64 v74, 0, v74, s[4:5]
	s_cselect_b64 s[4:5], -1, 0
	s_and_b64 s[4:5], vcc, s[4:5]
	s_cmp_lt_i32 s46, s76
	ds_write2_b32 v12, v21, v20 offset1:65
	ds_write2_b32 v12, v19, v18 offset0:130 offset1:195
	v_add_u32_e32 v18, 0x400, v12
	s_waitcnt vmcnt(5)
	v_cndmask_b32_e64 v73, 0, v73, s[4:5]
	s_cselect_b64 s[4:5], -1, 0
	ds_write2_b32 v18, v17, v16 offset0:4 offset1:69
	ds_write2_b32 v18, v15, v8 offset0:134 offset1:199
	v_add_u32_e32 v8, 0x800, v12
	s_and_b64 s[4:5], vcc, s[4:5]
	ds_write2_b32 v8, v29, v28 offset0:8 offset1:73
	ds_write2_b32 v8, v27, v26 offset0:138 offset1:203
	v_add_u32_e32 v8, 0xc00, v12
	s_cmp_lt_i32 s47, s76
	ds_write2_b32 v8, v25, v24 offset0:12 offset1:77
	ds_write2_b32 v8, v23, v22 offset0:142 offset1:207
	v_add_u32_e32 v8, 0x1000, v12
	s_waitcnt vmcnt(4)
	v_cndmask_b32_e64 v72, 0, v72, s[4:5]
	s_cselect_b64 s[4:5], -1, 0
	ds_write2_b32 v8, v37, v36 offset0:16 offset1:81
	ds_write2_b32 v8, v35, v34 offset0:146 offset1:211
	v_add_u32_e32 v8, 0x1400, v12
	s_and_b64 s[4:5], vcc, s[4:5]
	ds_write2_b32 v8, v33, v32 offset0:20 offset1:85
	ds_write2_b32 v8, v31, v30 offset0:150 offset1:215
	v_add_u32_e32 v8, 0x1800, v12
	s_cmp_lt_i32 s48, s76
	ds_write2_b32 v8, v45, v44 offset0:24 offset1:89
	ds_write2_b32 v8, v43, v42 offset0:154 offset1:219
	v_add_u32_e32 v8, 0x1c00, v12
	s_waitcnt vmcnt(3)
	v_cndmask_b32_e64 v71, 0, v71, s[4:5]
	s_cselect_b64 s[4:5], -1, 0
	ds_write2_b32 v8, v41, v40 offset0:28 offset1:93
	ds_write2_b32 v8, v39, v38 offset0:158 offset1:223
	v_add_u32_e32 v8, 0x2000, v12
	s_and_b64 s[4:5], vcc, s[4:5]
	ds_write2_b32 v8, v53, v52 offset0:32 offset1:97
	ds_write2_b32 v8, v51, v50 offset0:162 offset1:227
	v_add_u32_e32 v8, 0x2400, v12
	s_cmp_lt_i32 s49, s76
	ds_write2_b32 v8, v49, v48 offset0:36 offset1:101
	ds_write2_b32 v8, v47, v46 offset0:166 offset1:231
	v_add_u32_e32 v8, 0x2800, v12
	s_waitcnt vmcnt(2)
	v_cndmask_b32_e64 v77, 0, v77, s[4:5]
	s_cselect_b64 s[4:5], -1, 0
	ds_write2_b32 v8, v61, v60 offset0:40 offset1:105
	ds_write2_b32 v8, v59, v58 offset0:170 offset1:235
	v_add_u32_e32 v8, 0x2c00, v12
	s_and_b64 s[4:5], vcc, s[4:5]
	ds_write2_b32 v8, v57, v56 offset0:44 offset1:109
	ds_write2_b32 v8, v55, v54 offset0:174 offset1:239
	v_add_u32_e32 v8, 0x3000, v12
	s_cmp_lt_i32 s44, s76
	ds_write2_b32 v8, v70, v69 offset0:48 offset1:113
	ds_write2_b32 v8, v68, v67 offset0:178 offset1:243
	v_add_u32_e32 v8, 0x3400, v12
	s_waitcnt vmcnt(1)
	v_cndmask_b32_e64 v76, 0, v76, s[4:5]
	s_cselect_b64 s[4:5], -1, 0
	ds_write2_b32 v8, v66, v64 offset0:52 offset1:117
	ds_write2_b32 v8, v63, v62 offset0:182 offset1:247
	v_add_u32_e32 v8, 0x3800, v12
	s_and_b64 vcc, vcc, s[4:5]
	ds_write2_b32 v8, v65, v74 offset0:56 offset1:121
	ds_write2_b32 v8, v73, v72 offset0:186 offset1:251
	v_add_u32_e32 v8, 0x3c00, v12
	s_waitcnt vmcnt(0)
	v_cndmask_b32_e32 v75, 0, v75, vcc
	ds_write2_b32 v8, v71, v77 offset0:60 offset1:125
	ds_write2_b32 v8, v76, v75 offset0:190 offset1:255
	s_waitcnt lgkmcnt(0)
; __device__ __forceinline__ unsigned cvt_pk_bf16(float lo, float hi) { unsigned r; asm volatile("v_cvt_pk_bf16_f32 %0, %1, %2" : "=v"(r) : "v"(lo), "v"(hi)); return r; }
; #define LAS __attribute__((address_space(3)))
; #define LDS_WAIT() asm volatile("s_waitcnt lgkmcnt(0)" ::: "memory")
; __device__ __forceinline__ void conv_store(const ConvItem& ci, LAS float* scr, int lane, const float (&v)[64]) {
;     ...
;     LDS_WAIT(); asm volatile("" ::: "memory");
; #pragma unroll
;     for (int j = 0; j < 8; ++j) { const int n = (lane >> 3) + 8 * j; const LAS float* s = scr + (8 * c) * 65 + n;
;         v4u o; o.x = cvt_pk_bf16(s[0 * 65] * s0[0], s[1 * 65] * s0[1]); o.y = cvt_pk_bf16(s[2 * 65] * s0[2], s[3 * 65] * s0[3]); o.z = cvt_pk_bf16(s[4 * 65] * s1[0], s[5 * 65] * s1[1]); o.w = cvt_pk_bf16(s[6 * 65] * s1[2], s[7 * 65] * s1[3]);
;         *(v4u*)(ci.dst + (size_t)(ci.drow0 + n) * ci.ldd + ci.k0 + 8 * c) = o; }
	v_add_u32_e32 v192, 0x400, v14
	ds_read2_b32 v[128:129], v14 offset1:65
	ds_read2_b32 v[130:131], v14 offset0:130 offset1:195
	ds_read2_b32 v[132:133], v192 offset0:4 offset1:69
	ds_read2_b32 v[134:135], v192 offset0:134 offset1:199
	ds_read2_b32 v[136:137], v14 offset0:8 offset1:73
	ds_read2_b32 v[138:139], v14 offset0:138 offset1:203
	ds_read2_b32 v[140:141], v192 offset0:12 offset1:77
	ds_read2_b32 v[142:143], v192 offset0:142 offset1:207
	ds_read2_b32 v[144:145], v14 offset0:16 offset1:81
	ds_read2_b32 v[146:147], v14 offset0:146 offset1:211
	ds_read2_b32 v[148:149], v192 offset0:20 offset1:85
	ds_read2_b32 v[150:151], v192 offset0:150 offset1:215
	ds_read2_b32 v[152:153], v14 offset0:24 offset1:89
	ds_read2_b32 v[154:155], v14 offset0:154 offset1:219
	ds_read2_b32 v[156:157], v192 offset0:28 offset1:93
	ds_read2_b32 v[158:159], v192 offset0:158 offset1:223
	ds_read2_b32 v[160:161], v14 offset0:32 offset1:97
	ds_read2_b32 v[162:163], v14 offset0:162 offset1:227
	ds_read2_b32 v[164:165], v192 offset0:36 offset1:101
	ds_read2_b32 v[166:167], v192 offset0:166 offset1:231
	ds_read2_b32 v[168:169], v14 offset0:40 offset1:105
	ds_read2_b32 v[170:171], v14 offset0:170 offset1:235
	ds_read2_b32 v[172:173], v192 offset0:44 offset1:109
	ds_read2_b32 v[174:175], v192 offset0:174 offset1:239
	ds_read2_b32 v[176:177], v14 offset0:48 offset1:113
	ds_read2_b32 v[178:179], v14 offset0:178 offset1:243
	ds_read2_b32 v[180:181], v192 offset0:52 offset1:117
	ds_read2_b32 v[182:183], v192 offset0:182 offset1:247
	ds_read2_b32 v[184:185], v14 offset0:56 offset1:121
	ds_read2_b32 v[186:187], v14 offset0:186 offset1:251
	ds_read2_b32 v[188:189], v192 offset0:60 offset1:125
	ds_read2_b32 v[190:191], v192 offset0:190 offset1:255
	s_waitcnt lgkmcnt(0)
	v_add_u32_e32 v24, s59, v13
	v_mul_lo_u32 v22, s57, v24
	s_ashr_i32 s59, s58, 31
	v_readlane_b32 s76, v254, 31
	s_waitcnt lgkmcnt(0)
	v_mul_f32_e32 v8, v4, v128
	v_mul_f32_e32 v15, v5, v129
	v_cvt_pk_bf16_f32 v16, v8, v15
	s_add_i32 s3, s3, s33
	s_add_i32 s66, s66, s67
	s_add_i32 s68, s68, s69
	s_add_i32 s70, s70, s71
	s_waitcnt lgkmcnt(0)
	v_mul_f32_e32 v15, v7, v131
	v_mul_f32_e32 v8, v6, v130
	v_cvt_pk_bf16_f32 v17, v8, v15
	v_add_u32_e32 v15, 0x400, v14
	s_add_i32 s72, s72, s73
	s_add_i32 s74, s74, s75
	v_readlane_b32 s78, v254, 33
	v_readlane_b32 s79, v254, 34
	s_waitcnt lgkmcnt(0)
	v_mul_f32_e32 v8, v0, v132
	v_mul_f32_e32 v18, v1, v133
	v_cvt_pk_bf16_f32 v18, v8, v18
	v_readlane_b32 s80, v255, 21
	v_readlane_b32 s77, v254, 32
	s_movk_i32 s78, 0x1580
	v_readlane_b32 s82, v255, 23
	s_waitcnt lgkmcnt(0)
	v_mul_f32_e32 v8, v2, v134
	v_mul_f32_e32 v19, v3, v135
	v_cvt_pk_bf16_f32 v19, v8, v19
	v_ashrrev_i32_e32 v8, 31, v24
	v_mul_lo_u32 v8, s56, v8
	v_mad_u64_u32 v[20:21], s[4:5], s56, v24, 0
	v_add3_u32 v21, v21, v8, v22
	v_lshl_add_u64 v[20:21], v[20:21], 1, s[60:61]
	s_lshl_b64 s[4:5], s[58:59], 1
	v_lshl_add_u64 v[20:21], v[20:21], 0, s[4:5]
	v_lshlrev_b32_e32 v8, 1, v10
	v_lshl_add_u64 v[20:21], v[20:21], 0, v[8:9]
	global_store_dwordx4 v[20:21], v[16:19], off sc1 nt
	s_cmpk_lt_i32 s3, 21440
	v_readlane_b32 s83, v255, 24
	s_waitcnt lgkmcnt(0)
	v_mul_f32_e32 v16, v4, v136
	v_mul_f32_e32 v17, v5, v137
	v_cvt_pk_bf16_f32 v16, v16, v17
	s_mov_b32 s79, 0x3f22f983
	s_mov_b32 s85, 0xbfc90fda
	s_brev_b32 s86, 1
	s_movk_i32 s87, 0x1f8
	s_waitcnt lgkmcnt(0)
	v_mul_f32_e32 v17, v6, v138
	v_mul_f32_e32 v18, v7, v139
	v_cvt_pk_bf16_f32 v17, v17, v18
	s_mov_b64 s[88:89], 0x80
	s_mov_b64 s[92:93], 0x4000
	s_mov_b64 s[94:95], 0x4800
	v_readlane_b32 s81, v255, 22
	s_waitcnt lgkmcnt(0)
	v_mul_f32_e32 v18, v0, v140
	v_mul_f32_e32 v19, v1, v141
	v_cvt_pk_bf16_f32 v18, v18, v19
	s_waitcnt lgkmcnt(0)
	v_mul_f32_e32 v19, v2, v142
	v_mul_f32_e32 v20, v3, v143
	v_cvt_pk_bf16_f32 v19, v19, v20
	v_add_u32_e32 v20, 8, v24
	v_ashrrev_i32_e32 v21, 31, v20
	v_mul_lo_u32 v22, s56, v21
	v_mul_lo_u32 v23, s57, v20
	v_mad_u64_u32 v[20:21], s[6:7], s56, v20, 0
	v_add3_u32 v21, v21, v22, v23
	v_lshl_add_u64 v[20:21], v[20:21], 1, s[60:61]
	v_lshl_add_u64 v[20:21], v[20:21], 0, s[4:5]
	v_lshl_add_u64 v[20:21], v[20:21], 0, v[8:9]
	global_store_dwordx4 v[20:21], v[16:19], off sc1 nt
	s_waitcnt lgkmcnt(0)
	s_nop 0
	v_mul_f32_e32 v16, v4, v144
	v_mul_f32_e32 v17, v5, v145
	v_cvt_pk_bf16_f32 v16, v16, v17
	s_waitcnt lgkmcnt(0)
	v_mul_f32_e32 v17, v6, v146
	v_mul_f32_e32 v18, v7, v147
	v_cvt_pk_bf16_f32 v17, v17, v18
	s_waitcnt lgkmcnt(0)
	v_mul_f32_e32 v18, v0, v148
	v_mul_f32_e32 v19, v1, v149
	v_cvt_pk_bf16_f32 v18, v18, v19
	s_waitcnt lgkmcnt(0)
; __device__ __forceinline__ unsigned cvt_pk_bf16(float lo, float hi) { unsigned r; asm volatile("v_cvt_pk_bf16_f32 %0, %1, %2" : "=v"(r) : "v"(lo), "v"(hi)); return r; }
; #define LAS __attribute__((address_space(3)))
; __device__ __forceinline__ void conv_store(const ConvItem& ci, LAS float* scr, int lane, const float (&v)[64]) {
;     ...
;     for (int j = 0; j < 8; ++j) { const int n = (lane >> 3) + 8 * j; const LAS float* s = scr + (8 * c) * 65 + n;
;         v4u o; o.x = cvt_pk_bf16(s[0 * 65] * s0[0], s[1 * 65] * s0[1]); o.y = cvt_pk_bf16(s[2 * 65] * s0[2], s[3 * 65] * s0[3]); o.z = cvt_pk_bf16(s[4 * 65] * s1[0], s[5 * 65] * s1[1]); o.w = cvt_pk_bf16(s[6 * 65] * s1[2], s[7 * 65] * s1[3]);
;         *(v4u*)(ci.dst + (size_t)(ci.drow0 + n) * ci.ldd + ci.k0 + 8 * c) = o; }
	v_mul_f32_e32 v19, v2, v150
	v_mul_f32_e32 v20, v3, v151
	v_cvt_pk_bf16_f32 v19, v19, v20
	v_add_u32_e32 v20, 16, v24
	v_ashrrev_i32_e32 v21, 31, v20
	v_mul_lo_u32 v22, s56, v21
	v_mul_lo_u32 v23, s57, v20
	v_mad_u64_u32 v[20:21], s[6:7], s56, v20, 0
	v_add3_u32 v21, v21, v22, v23
	v_lshl_add_u64 v[20:21], v[20:21], 1, s[60:61]
	v_lshl_add_u64 v[20:21], v[20:21], 0, s[4:5]
	v_lshl_add_u64 v[20:21], v[20:21], 0, v[8:9]
	global_store_dwordx4 v[20:21], v[16:19], off sc1 nt
	s_waitcnt lgkmcnt(0)
	s_nop 0
	v_mul_f32_e32 v16, v4, v152
	v_mul_f32_e32 v17, v5, v153
	v_cvt_pk_bf16_f32 v16, v16, v17
	s_waitcnt lgkmcnt(0)
	v_mul_f32_e32 v17, v6, v154
	v_mul_f32_e32 v18, v7, v155
	v_cvt_pk_bf16_f32 v17, v17, v18
	s_waitcnt lgkmcnt(0)
	v_mul_f32_e32 v18, v0, v156
	v_mul_f32_e32 v19, v1, v157
	v_cvt_pk_bf16_f32 v18, v18, v19
	s_waitcnt lgkmcnt(0)
	v_mul_f32_e32 v19, v2, v158
	v_mul_f32_e32 v20, v3, v159
	v_cvt_pk_bf16_f32 v19, v19, v20
	v_add_u32_e32 v20, 24, v24
	v_ashrrev_i32_e32 v21, 31, v20
	v_mul_lo_u32 v22, s56, v21
	v_mul_lo_u32 v23, s57, v20
	v_mad_u64_u32 v[20:21], s[6:7], s56, v20, 0
	v_add3_u32 v21, v21, v22, v23
	v_lshl_add_u64 v[20:21], v[20:21], 1, s[60:61]
	v_lshl_add_u64 v[20:21], v[20:21], 0, s[4:5]
	v_lshl_add_u64 v[20:21], v[20:21], 0, v[8:9]
	global_store_dwordx4 v[20:21], v[16:19], off sc1 nt
	s_waitcnt lgkmcnt(0)
	s_nop 0
	v_mul_f32_e32 v16, v4, v160
	v_mul_f32_e32 v17, v5, v161
	v_cvt_pk_bf16_f32 v16, v16, v17
	s_waitcnt lgkmcnt(0)
	v_mul_f32_e32 v17, v6, v162
	v_mul_f32_e32 v18, v7, v163
	v_cvt_pk_bf16_f32 v17, v17, v18
	s_waitcnt lgkmcnt(0)
	v_mul_f32_e32 v18, v0, v164
	v_mul_f32_e32 v19, v1, v165
	v_cvt_pk_bf16_f32 v18, v18, v19
	s_waitcnt lgkmcnt(0)
	v_mul_f32_e32 v19, v2, v166
	v_mul_f32_e32 v20, v3, v167
	v_cvt_pk_bf16_f32 v19, v19, v20
	v_add_u32_e32 v20, 32, v24
	v_ashrrev_i32_e32 v21, 31, v20
	v_mul_lo_u32 v22, s56, v21
	v_mul_lo_u32 v23, s57, v20
	v_mad_u64_u32 v[20:21], s[6:7], s56, v20, 0
	v_add3_u32 v21, v21, v22, v23
	v_lshl_add_u64 v[20:21], v[20:21], 1, s[60:61]
	v_lshl_add_u64 v[20:21], v[20:21], 0, s[4:5]
	v_lshl_add_u64 v[20:21], v[20:21], 0, v[8:9]
	global_store_dwordx4 v[20:21], v[16:19], off sc1 nt
	s_waitcnt lgkmcnt(0)
	s_nop 0
	v_mul_f32_e32 v16, v4, v168
	v_mul_f32_e32 v17, v5, v169
	v_cvt_pk_bf16_f32 v16, v16, v17
	s_waitcnt lgkmcnt(0)
	v_mul_f32_e32 v17, v6, v170
	v_mul_f32_e32 v18, v7, v171
	v_cvt_pk_bf16_f32 v17, v17, v18
	s_waitcnt lgkmcnt(0)
	v_mul_f32_e32 v18, v0, v172
	v_mul_f32_e32 v19, v1, v173
	v_cvt_pk_bf16_f32 v18, v18, v19
	s_waitcnt lgkmcnt(0)
	v_mul_f32_e32 v19, v2, v174
	v_mul_f32_e32 v20, v3, v175
	v_cvt_pk_bf16_f32 v19, v19, v20
	v_add_u32_e32 v20, 40, v24
	v_ashrrev_i32_e32 v21, 31, v20
	v_mul_lo_u32 v22, s56, v21
	v_mul_lo_u32 v23, s57, v20
	v_mad_u64_u32 v[20:21], s[6:7], s56, v20, 0
	v_add3_u32 v21, v21, v22, v23
	v_lshl_add_u64 v[20:21], v[20:21], 1, s[60:61]
	v_lshl_add_u64 v[20:21], v[20:21], 0, s[4:5]
	v_lshl_add_u64 v[20:21], v[20:21], 0, v[8:9]
	global_store_dwordx4 v[20:21], v[16:19], off sc1 nt
	s_waitcnt lgkmcnt(0)
	s_nop 0
	v_mul_f32_e32 v16, v4, v176
	v_mul_f32_e32 v17, v5, v177
	v_cvt_pk_bf16_f32 v16, v16, v17
	s_waitcnt lgkmcnt(0)
	v_mul_f32_e32 v17, v6, v178
	v_mul_f32_e32 v18, v7, v179
	v_cvt_pk_bf16_f32 v17, v17, v18
	s_waitcnt lgkmcnt(0)
	v_mul_f32_e32 v18, v0, v180
	v_mul_f32_e32 v19, v1, v181
	v_cvt_pk_bf16_f32 v18, v18, v19
	s_waitcnt lgkmcnt(0)
	v_mul_f32_e32 v19, v2, v182
	v_mul_f32_e32 v20, v3, v183
	v_cvt_pk_bf16_f32 v19, v19, v20
	v_add_u32_e32 v20, 48, v24
	v_ashrrev_i32_e32 v21, 31, v20
	v_mul_lo_u32 v22, s56, v21
	v_mul_lo_u32 v23, s57, v20
	v_mad_u64_u32 v[20:21], s[6:7], s56, v20, 0
	v_add3_u32 v21, v21, v22, v23
	v_lshl_add_u64 v[20:21], v[20:21], 1, s[60:61]
	v_lshl_add_u64 v[20:21], v[20:21], 0, s[4:5]
	v_lshl_add_u64 v[20:21], v[20:21], 0, v[8:9]
	global_store_dwordx4 v[20:21], v[16:19], off sc1 nt
	s_waitcnt lgkmcnt(0)
	v_mul_f32_e32 v4, v4, v184
	v_mul_f32_e32 v5, v5, v185
	v_cvt_pk_bf16_f32 v4, v4, v5
	s_waitcnt lgkmcnt(0)
	v_mul_f32_e32 v5, v6, v186
	v_mul_f32_e32 v6, v7, v187
	v_cvt_pk_bf16_f32 v5, v5, v6
	s_waitcnt lgkmcnt(0)
	v_mul_f32_e32 v0, v0, v188
	v_mul_f32_e32 v1, v1, v189
	v_cvt_pk_bf16_f32 v6, v0, v1
	s_waitcnt lgkmcnt(0)
	v_mul_f32_e32 v0, v2, v190
	v_mul_f32_e32 v1, v3, v191
	v_cvt_pk_bf16_f32 v7, v0, v1
	v_add_u32_e32 v0, 56, v24
	v_ashrrev_i32_e32 v1, 31, v0
	v_mul_lo_u32 v2, s56, v1
	v_mul_lo_u32 v3, s57, v0
	v_mad_u64_u32 v[0:1], s[6:7], s56, v0, 0
	v_add3_u32 v1, v1, v2, v3
	v_lshl_add_u64 v[0:1], v[0:1], 1, s[60:61]
	v_lshl_add_u64 v[0:1], v[0:1], 0, s[4:5]
	v_lshl_add_u64 v[0:1], v[0:1], 0, v[8:9]
	global_store_dwordx4 v[0:1], v[4:7], off sc1 nt
	s_waitcnt lgkmcnt(0)
	s_cbranch_scc0 .Lcvp30_ret

; __device__ __forceinline__ void conv_load(const ConvItem& ci, int lane, float (&v)[64]) {
;     const bool okc = ci.srcc >= 0 && (ci.srcc + lane) < ci.ncols;
;     const float* base = ci.W + (okc ? ci.srcc + lane : 0);
;     const int kmax = ci.Ksrc - 1;
; #pragma unroll
;     for (int i = 0; i < 64; ++i) { const int k = ci.k0 + i, kk = k < kmax ? k : kmax; v[i] = __builtin_nontemporal_load(base + (size_t)kk * ci.ldw); }
; #pragma unroll
;     for (int i = 0; i < 64; ++i) v[i] = (okc && (ci.k0 + i) < ci.Ksrc) ? v[i] : 0.f;
.Lcvp31_30:
	s_cmp_lt_i32 s58, s76
	s_cselect_b64 s[4:5], -1, 0
	s_and_b64 s[4:5], vcc, s[4:5]
	s_cmp_lt_i32 s64, s76
	s_waitcnt vmcnt(62)
	v_cndmask_b32_e64 v21, 0, v21, s[4:5]
	s_cselect_b64 s[4:5], -1, 0
	s_and_b64 s[4:5], vcc, s[4:5]
	s_cmp_lt_i32 s65, s76
	v_cndmask_b32_e64 v20, 0, v20, s[4:5]
	s_cselect_b64 s[4:5], -1, 0
	s_and_b64 s[4:5], vcc, s[4:5]
	s_cmp_lt_i32 s78, s76
	s_waitcnt vmcnt(61)
	v_cndmask_b32_e64 v19, 0, v19, s[4:5]
	s_cselect_b64 s[4:5], -1, 0
	s_and_b64 s[4:5], vcc, s[4:5]
	s_cmp_lt_i32 s79, s76
	s_waitcnt vmcnt(60)
	v_cndmask_b32_e64 v18, 0, v18, s[4:5]
	s_cselect_b64 s[4:5], -1, 0
	s_and_b64 s[4:5], vcc, s[4:5]
	s_cmp_lt_i32 s80, s76
	s_waitcnt vmcnt(59)
	v_cndmask_b32_e64 v17, 0, v17, s[4:5]
	s_cselect_b64 s[4:5], -1, 0
	s_and_b64 s[4:5], vcc, s[4:5]
	s_cmp_lt_i32 s81, s76
	s_waitcnt vmcnt(58)
	v_cndmask_b32_e64 v16, 0, v16, s[4:5]
	s_cselect_b64 s[4:5], -1, 0
	s_and_b64 s[4:5], vcc, s[4:5]
	s_cmp_lt_i32 s82, s76
	s_waitcnt vmcnt(57)
	v_cndmask_b32_e64 v15, 0, v15, s[4:5]
	s_cselect_b64 s[4:5], -1, 0
	s_and_b64 s[4:5], vcc, s[4:5]
	s_cmp_lt_i32 s83, s76
	s_waitcnt vmcnt(56)
	v_cndmask_b32_e64 v8, 0, v8, s[4:5]
	s_cselect_b64 s[4:5], -1, 0
	s_and_b64 s[4:5], vcc, s[4:5]
	s_cmp_lt_i32 s85, s76
	s_waitcnt vmcnt(55)
	v_cndmask_b32_e64 v29, 0, v29, s[4:5]
	s_cselect_b64 s[4:5], -1, 0
	s_and_b64 s[4:5], vcc, s[4:5]
	s_cmp_lt_i32 s86, s76
	s_waitcnt vmcnt(54)
	v_cndmask_b32_e64 v28, 0, v28, s[4:5]
	s_cselect_b64 s[4:5], -1, 0
	s_and_b64 s[4:5], vcc, s[4:5]
	s_cmp_lt_i32 s87, s76
	s_waitcnt vmcnt(53)
	v_cndmask_b32_e64 v27, 0, v27, s[4:5]
	s_cselect_b64 s[4:5], -1, 0
	s_and_b64 s[4:5], vcc, s[4:5]
	s_cmp_lt_i32 s88, s76
	s_waitcnt vmcnt(52)
	v_cndmask_b32_e64 v26, 0, v26, s[4:5]
	s_cselect_b64 s[4:5], -1, 0
	s_and_b64 s[4:5], vcc, s[4:5]
	s_cmp_lt_i32 s89, s76
	s_waitcnt vmcnt(51)
	v_cndmask_b32_e64 v25, 0, v25, s[4:5]
	s_cselect_b64 s[4:5], -1, 0
	s_and_b64 s[4:5], vcc, s[4:5]
	s_cmp_lt_i32 s90, s76
	s_waitcnt vmcnt(50)
	v_cndmask_b32_e64 v24, 0, v24, s[4:5]
	s_cselect_b64 s[4:5], -1, 0
	s_and_b64 s[4:5], vcc, s[4:5]
	s_cmp_lt_i32 s92, s76
	s_waitcnt vmcnt(49)
	v_cndmask_b32_e64 v23, 0, v23, s[4:5]
	s_cselect_b64 s[4:5], -1, 0
	s_and_b64 s[4:5], vcc, s[4:5]
	s_cmp_lt_i32 s93, s76
	s_waitcnt vmcnt(48)
	v_cndmask_b32_e64 v22, 0, v22, s[4:5]
	s_cselect_b64 s[4:5], -1, 0
	s_and_b64 s[4:5], vcc, s[4:5]
	s_cmp_lt_i32 s94, s76
	s_waitcnt vmcnt(47)
	v_cndmask_b32_e64 v37, 0, v37, s[4:5]
	s_cselect_b64 s[4:5], -1, 0
	s_and_b64 s[4:5], vcc, s[4:5]
	s_cmp_lt_i32 s95, s76
	s_waitcnt vmcnt(46)
	v_cndmask_b32_e64 v36, 0, v36, s[4:5]
	s_cselect_b64 s[4:5], -1, 0
	s_and_b64 s[4:5], vcc, s[4:5]
	s_cmp_lt_i32 s50, s76
	s_waitcnt vmcnt(45)
	v_cndmask_b32_e64 v35, 0, v35, s[4:5]
	s_cselect_b64 s[4:5], -1, 0
	s_and_b64 s[4:5], vcc, s[4:5]
	s_cmp_lt_i32 s51, s76
	s_waitcnt vmcnt(44)
	v_cndmask_b32_e64 v34, 0, v34, s[4:5]
	s_cselect_b64 s[4:5], -1, 0
	s_and_b64 s[4:5], vcc, s[4:5]
	s_cmp_lt_i32 s52, s76
	s_waitcnt vmcnt(43)
	v_cndmask_b32_e64 v33, 0, v33, s[4:5]
	s_cselect_b64 s[4:5], -1, 0
	s_and_b64 s[4:5], vcc, s[4:5]
	s_cmp_lt_i32 s53, s76
	s_waitcnt vmcnt(42)
	v_cndmask_b32_e64 v32, 0, v32, s[4:5]
	s_cselect_b64 s[4:5], -1, 0
	s_and_b64 s[4:5], vcc, s[4:5]
	s_cmp_lt_i32 s6, s76
	s_waitcnt vmcnt(41)
	v_cndmask_b32_e64 v31, 0, v31, s[4:5]
	s_cselect_b64 s[4:5], -1, 0
	s_and_b64 s[4:5], vcc, s[4:5]
	s_cmp_lt_i32 s7, s76
	s_waitcnt vmcnt(40)
	v_cndmask_b32_e64 v30, 0, v30, s[4:5]
	s_cselect_b64 s[4:5], -1, 0
	s_and_b64 s[4:5], vcc, s[4:5]
	s_cmp_lt_i32 s8, s76
	s_waitcnt vmcnt(39)
	v_cndmask_b32_e64 v45, 0, v45, s[4:5]
	s_cselect_b64 s[4:5], -1, 0
	s_and_b64 s[4:5], vcc, s[4:5]
	s_cmp_lt_i32 s9, s76
	s_waitcnt vmcnt(38)
	v_cndmask_b32_e64 v44, 0, v44, s[4:5]
	s_cselect_b64 s[4:5], -1, 0
	s_and_b64 s[4:5], vcc, s[4:5]
	s_cmp_lt_i32 s10, s76
	s_waitcnt vmcnt(37)
	v_cndmask_b32_e64 v43, 0, v43, s[4:5]
	s_cselect_b64 s[4:5], -1, 0
	s_and_b64 s[4:5], vcc, s[4:5]
	s_cmp_lt_i32 s11, s76
	s_waitcnt vmcnt(36)
	v_cndmask_b32_e64 v42, 0, v42, s[4:5]
	s_cselect_b64 s[4:5], -1, 0
	s_and_b64 s[4:5], vcc, s[4:5]
	s_cmp_lt_i32 s14, s76
	s_waitcnt vmcnt(35)
	v_cndmask_b32_e64 v41, 0, v41, s[4:5]
	s_cselect_b64 s[4:5], -1, 0
	s_and_b64 s[4:5], vcc, s[4:5]
	s_cmp_lt_i32 s15, s76
	s_waitcnt vmcnt(34)
	v_cndmask_b32_e64 v40, 0, v40, s[4:5]
	s_cselect_b64 s[4:5], -1, 0
	s_and_b64 s[4:5], vcc, s[4:5]
	s_cmp_lt_i32 s16, s76
	s_waitcnt vmcnt(33)
	v_cndmask_b32_e64 v39, 0, v39, s[4:5]
	s_cselect_b64 s[4:5], -1, 0
	s_and_b64 s[4:5], vcc, s[4:5]
	s_cmp_lt_i32 s17, s76
	s_waitcnt vmcnt(32)
	v_cndmask_b32_e64 v38, 0, v38, s[4:5]
	s_cselect_b64 s[4:5], -1, 0
	s_and_b64 s[4:5], vcc, s[4:5]
	s_cmp_lt_i32 s12, s76
	s_waitcnt vmcnt(31)
	v_cndmask_b32_e64 v53, 0, v53, s[4:5]
	s_cselect_b64 s[4:5], -1, 0
	s_and_b64 s[4:5], vcc, s[4:5]
	s_cmp_lt_i32 s13, s76
	s_waitcnt vmcnt(30)
	v_cndmask_b32_e64 v52, 0, v52, s[4:5]
	s_cselect_b64 s[4:5], -1, 0
	s_and_b64 s[4:5], vcc, s[4:5]
	s_cmp_lt_i32 s20, s76
	s_waitcnt vmcnt(29)
	v_cndmask_b32_e64 v51, 0, v51, s[4:5]
	s_cselect_b64 s[4:5], -1, 0
	s_and_b64 s[4:5], vcc, s[4:5]
	s_cmp_lt_i32 s21, s76
	s_waitcnt vmcnt(28)
	v_cndmask_b32_e64 v50, 0, v50, s[4:5]
	s_cselect_b64 s[4:5], -1, 0
	s_and_b64 s[4:5], vcc, s[4:5]
	s_cmp_lt_i32 s24, s76
	s_waitcnt vmcnt(27)
	v_cndmask_b32_e64 v49, 0, v49, s[4:5]
	s_cselect_b64 s[4:5], -1, 0
	s_and_b64 s[4:5], vcc, s[4:5]
	s_cmp_lt_i32 s25, s76
	s_waitcnt vmcnt(26)
	v_cndmask_b32_e64 v48, 0, v48, s[4:5]
	s_cselect_b64 s[4:5], -1, 0
	s_and_b64 s[4:5], vcc, s[4:5]
	s_cmp_lt_i32 s26, s76
	s_waitcnt vmcnt(25)
	v_cndmask_b32_e64 v47, 0, v47, s[4:5]
	s_cselect_b64 s[4:5], -1, 0
	s_and_b64 s[4:5], vcc, s[4:5]
	s_cmp_lt_i32 s27, s76
	s_waitcnt vmcnt(24)
; #define LAS __attribute__((address_space(3)))
; #define LDS_WAIT() asm volatile("s_waitcnt lgkmcnt(0)" ::: "memory")
; __device__ __forceinline__ void conv_load(const ConvItem& ci, int lane, float (&v)[64]) {
;     ...
;     for (int i = 0; i < 64; ++i) v[i] = (okc && (ci.k0 + i) < ci.Ksrc) ? v[i] : 0.f;
; }
; __device__ __forceinline__ void conv_store(const ConvItem& ci, LAS float* scr, int lane, const float (&v)[64]) {
;     const int c = lane & 7;
;     f32x4 s0 = {1.f, 1.f, 1.f, 1.f}, s1 = s0;
;     if (ci.ks) { const int kb = ci.k0 + 8 * c < ci.Ksrc - 8 ? ci.k0 + 8 * c : ci.Ksrc - 8; s0 = *(const f32x4*)(ci.ks + kb); s1 = *(const f32x4*)(ci.ks + kb + 4); }
; #pragma unroll
;     for (int i = 0; i < 64; ++i) scr[i * 65 + lane] = v[i];
;     LDS_WAIT(); asm volatile("" ::: "memory");
	v_cndmask_b32_e64 v46, 0, v46, s[4:5]
	s_cselect_b64 s[4:5], -1, 0
	s_and_b64 s[4:5], vcc, s[4:5]
	s_cmp_lt_i32 s18, s76
	s_waitcnt vmcnt(23)
	v_cndmask_b32_e64 v61, 0, v61, s[4:5]
	s_cselect_b64 s[4:5], -1, 0
	s_and_b64 s[4:5], vcc, s[4:5]
	s_cmp_lt_i32 s19, s76
	s_waitcnt vmcnt(22)
	v_cndmask_b32_e64 v60, 0, v60, s[4:5]
	s_cselect_b64 s[4:5], -1, 0
	s_and_b64 s[4:5], vcc, s[4:5]
	s_cmp_lt_i32 s28, s76
	s_waitcnt vmcnt(21)
	v_cndmask_b32_e64 v59, 0, v59, s[4:5]
	s_cselect_b64 s[4:5], -1, 0
	s_and_b64 s[4:5], vcc, s[4:5]
	s_cmp_lt_i32 s29, s76
	s_waitcnt vmcnt(20)
	v_cndmask_b32_e64 v58, 0, v58, s[4:5]
	s_cselect_b64 s[4:5], -1, 0
	s_and_b64 s[4:5], vcc, s[4:5]
	s_cmp_lt_i32 s22, s76
	s_waitcnt vmcnt(19)
	v_cndmask_b32_e64 v57, 0, v57, s[4:5]
	s_cselect_b64 s[4:5], -1, 0
	s_and_b64 s[4:5], vcc, s[4:5]
	s_cmp_lt_i32 s23, s76
	s_waitcnt vmcnt(18)
	v_cndmask_b32_e64 v56, 0, v56, s[4:5]
	s_cselect_b64 s[4:5], -1, 0
	s_and_b64 s[4:5], vcc, s[4:5]
	s_cmp_lt_i32 s30, s76
	s_waitcnt vmcnt(17)
	v_cndmask_b32_e64 v55, 0, v55, s[4:5]
	s_cselect_b64 s[4:5], -1, 0
	s_and_b64 s[4:5], vcc, s[4:5]
	s_cmp_lt_i32 s31, s76
	s_waitcnt vmcnt(16)
	v_cndmask_b32_e64 v54, 0, v54, s[4:5]
	s_cselect_b64 s[4:5], -1, 0
	s_and_b64 s[4:5], vcc, s[4:5]
	s_cmp_lt_i32 s36, s76
	s_waitcnt vmcnt(15)
	v_cndmask_b32_e64 v70, 0, v70, s[4:5]
	s_cselect_b64 s[4:5], -1, 0
	s_and_b64 s[4:5], vcc, s[4:5]
	s_cmp_lt_i32 s37, s76
	s_waitcnt vmcnt(14)
	v_cndmask_b32_e64 v69, 0, v69, s[4:5]
	s_cselect_b64 s[4:5], -1, 0
	s_and_b64 s[4:5], vcc, s[4:5]
	s_cmp_lt_i32 s38, s76
	s_waitcnt vmcnt(13)
	v_cndmask_b32_e64 v68, 0, v68, s[4:5]
	s_cselect_b64 s[4:5], -1, 0
	s_and_b64 s[4:5], vcc, s[4:5]
	s_cmp_lt_i32 s39, s76
	s_waitcnt vmcnt(12)
	v_cndmask_b32_e64 v67, 0, v67, s[4:5]
	s_cselect_b64 s[4:5], -1, 0
	s_and_b64 s[4:5], vcc, s[4:5]
	s_cmp_lt_i32 s34, s76
	s_waitcnt vmcnt(11)
	v_cndmask_b32_e64 v66, 0, v66, s[4:5]
	s_cselect_b64 s[4:5], -1, 0
	s_and_b64 s[4:5], vcc, s[4:5]
	s_cmp_lt_i32 s35, s76
	s_waitcnt vmcnt(10)
	v_cndmask_b32_e64 v64, 0, v64, s[4:5]
	s_cselect_b64 s[4:5], -1, 0
	s_and_b64 s[4:5], vcc, s[4:5]
	s_cmp_lt_i32 s42, s76
	s_waitcnt vmcnt(9)
	v_cndmask_b32_e64 v63, 0, v63, s[4:5]
	s_cselect_b64 s[4:5], -1, 0
	s_and_b64 s[4:5], vcc, s[4:5]
	s_cmp_lt_i32 s43, s76
	s_waitcnt vmcnt(8)
	v_cndmask_b32_e64 v62, 0, v62, s[4:5]
	s_cselect_b64 s[4:5], -1, 0
	s_and_b64 s[4:5], vcc, s[4:5]
	s_cmp_lt_i32 s54, s76
	s_waitcnt vmcnt(7)
	v_cndmask_b32_e64 v65, 0, v65, s[4:5]
	s_cselect_b64 s[4:5], -1, 0
	s_and_b64 s[4:5], vcc, s[4:5]
	s_cmp_lt_i32 s55, s76
	s_waitcnt vmcnt(6)
	v_cndmask_b32_e64 v74, 0, v74, s[4:5]
	s_cselect_b64 s[4:5], -1, 0
	s_and_b64 s[4:5], vcc, s[4:5]
	s_cmp_lt_i32 s46, s76
	ds_write2_b32 v12, v21, v20 offset1:65
	ds_write2_b32 v12, v19, v18 offset0:130 offset1:195
	v_add_u32_e32 v18, 0x400, v12
	s_waitcnt vmcnt(5)
	v_cndmask_b32_e64 v73, 0, v73, s[4:5]
	s_cselect_b64 s[4:5], -1, 0
	ds_write2_b32 v18, v17, v16 offset0:4 offset1:69
	ds_write2_b32 v18, v15, v8 offset0:134 offset1:199
	v_add_u32_e32 v8, 0x800, v12
	s_and_b64 s[4:5], vcc, s[4:5]
	ds_write2_b32 v8, v29, v28 offset0:8 offset1:73
	ds_write2_b32 v8, v27, v26 offset0:138 offset1:203
	v_add_u32_e32 v8, 0xc00, v12
	s_cmp_lt_i32 s47, s76
	ds_write2_b32 v8, v25, v24 offset0:12 offset1:77
	ds_write2_b32 v8, v23, v22 offset0:142 offset1:207
	v_add_u32_e32 v8, 0x1000, v12
	s_waitcnt vmcnt(4)
	v_cndmask_b32_e64 v72, 0, v72, s[4:5]
	s_cselect_b64 s[4:5], -1, 0
	ds_write2_b32 v8, v37, v36 offset0:16 offset1:81
	ds_write2_b32 v8, v35, v34 offset0:146 offset1:211
	v_add_u32_e32 v8, 0x1400, v12
	s_and_b64 s[4:5], vcc, s[4:5]
	ds_write2_b32 v8, v33, v32 offset0:20 offset1:85
	ds_write2_b32 v8, v31, v30 offset0:150 offset1:215
	v_add_u32_e32 v8, 0x1800, v12
	s_cmp_lt_i32 s48, s76
	ds_write2_b32 v8, v45, v44 offset0:24 offset1:89
	ds_write2_b32 v8, v43, v42 offset0:154 offset1:219
	v_add_u32_e32 v8, 0x1c00, v12
	s_waitcnt vmcnt(3)
	v_cndmask_b32_e64 v71, 0, v71, s[4:5]
	s_cselect_b64 s[4:5], -1, 0
	ds_write2_b32 v8, v41, v40 offset0:28 offset1:93
	ds_write2_b32 v8, v39, v38 offset0:158 offset1:223
	v_add_u32_e32 v8, 0x2000, v12
	s_and_b64 s[4:5], vcc, s[4:5]
	ds_write2_b32 v8, v53, v52 offset0:32 offset1:97
	ds_write2_b32 v8, v51, v50 offset0:162 offset1:227
	v_add_u32_e32 v8, 0x2400, v12
	s_cmp_lt_i32 s49, s76
	ds_write2_b32 v8, v49, v48 offset0:36 offset1:101
	ds_write2_b32 v8, v47, v46 offset0:166 offset1:231
	v_add_u32_e32 v8, 0x2800, v12
	s_waitcnt vmcnt(2)
	v_cndmask_b32_e64 v77, 0, v77, s[4:5]
	s_cselect_b64 s[4:5], -1, 0
	ds_write2_b32 v8, v61, v60 offset0:40 offset1:105
	ds_write2_b32 v8, v59, v58 offset0:170 offset1:235
	v_add_u32_e32 v8, 0x2c00, v12
	s_and_b64 s[4:5], vcc, s[4:5]
	ds_write2_b32 v8, v57, v56 offset0:44 offset1:109
	ds_write2_b32 v8, v55, v54 offset0:174 offset1:239
	v_add_u32_e32 v8, 0x3000, v12
	s_cmp_lt_i32 s44, s76
	ds_write2_b32 v8, v70, v69 offset0:48 offset1:113
	ds_write2_b32 v8, v68, v67 offset0:178 offset1:243
	v_add_u32_e32 v8, 0x3400, v12
	s_waitcnt vmcnt(1)
	v_cndmask_b32_e64 v76, 0, v76, s[4:5]
	s_cselect_b64 s[4:5], -1, 0
	ds_write2_b32 v8, v66, v64 offset0:52 offset1:117
	ds_write2_b32 v8, v63, v62 offset0:182 offset1:247
	v_add_u32_e32 v8, 0x3800, v12
	s_and_b64 vcc, vcc, s[4:5]
	ds_write2_b32 v8, v65, v74 offset0:56 offset1:121
	ds_write2_b32 v8, v73, v72 offset0:186 offset1:251
	v_add_u32_e32 v8, 0x3c00, v12
	s_waitcnt vmcnt(0)
	v_cndmask_b32_e32 v75, 0, v75, vcc
	ds_write2_b32 v8, v71, v77 offset0:60 offset1:125
	ds_write2_b32 v8, v76, v75 offset0:190 offset1:255
	s_waitcnt lgkmcnt(0)
; __device__ __forceinline__ unsigned cvt_pk_bf16(float lo, float hi) { unsigned r; asm volatile("v_cvt_pk_bf16_f32 %0, %1, %2" : "=v"(r) : "v"(lo), "v"(hi)); return r; }
; #define LAS __attribute__((address_space(3)))
; #define LDS_WAIT() asm volatile("s_waitcnt lgkmcnt(0)" ::: "memory")
; __device__ __forceinline__ void conv_store(const ConvItem& ci, LAS float* scr, int lane, const float (&v)[64]) {
;     ...
;     LDS_WAIT(); asm volatile("" ::: "memory");
; #pragma unroll
;     for (int j = 0; j < 8; ++j) { const int n = (lane >> 3) + 8 * j; const LAS float* s = scr + (8 * c) * 65 + n;
;         v4u o; o.x = cvt_pk_bf16(s[0 * 65] * s0[0], s[1 * 65] * s0[1]); o.y = cvt_pk_bf16(s[2 * 65] * s0[2], s[3 * 65] * s0[3]); o.z = cvt_pk_bf16(s[4 * 65] * s1[0], s[5 * 65] * s1[1]); o.w = cvt_pk_bf16(s[6 * 65] * s1[2], s[7 * 65] * s1[3]);
;         *(v4u*)(ci.dst + (size_t)(ci.drow0 + n) * ci.ldd + ci.k0 + 8 * c) = o; }
	v_add_u32_e32 v192, 0x400, v14
	ds_read2_b32 v[128:129], v14 offset1:65
	ds_read2_b32 v[130:131], v14 offset0:130 offset1:195
	ds_read2_b32 v[132:133], v192 offset0:4 offset1:69
	ds_read2_b32 v[134:135], v192 offset0:134 offset1:199
	ds_read2_b32 v[136:137], v14 offset0:8 offset1:73
	ds_read2_b32 v[138:139], v14 offset0:138 offset1:203
	ds_read2_b32 v[140:141], v192 offset0:12 offset1:77
	ds_read2_b32 v[142:143], v192 offset0:142 offset1:207
	ds_read2_b32 v[144:145], v14 offset0:16 offset1:81
	ds_read2_b32 v[146:147], v14 offset0:146 offset1:211
	ds_read2_b32 v[148:149], v192 offset0:20 offset1:85
	ds_read2_b32 v[150:151], v192 offset0:150 offset1:215
	ds_read2_b32 v[152:153], v14 offset0:24 offset1:89
	ds_read2_b32 v[154:155], v14 offset0:154 offset1:219
	ds_read2_b32 v[156:157], v192 offset0:28 offset1:93
	ds_read2_b32 v[158:159], v192 offset0:158 offset1:223
	ds_read2_b32 v[160:161], v14 offset0:32 offset1:97
	ds_read2_b32 v[162:163], v14 offset0:162 offset1:227
	ds_read2_b32 v[164:165], v192 offset0:36 offset1:101
	ds_read2_b32 v[166:167], v192 offset0:166 offset1:231
	ds_read2_b32 v[168:169], v14 offset0:40 offset1:105
	ds_read2_b32 v[170:171], v14 offset0:170 offset1:235
	ds_read2_b32 v[172:173], v192 offset0:44 offset1:109
	ds_read2_b32 v[174:175], v192 offset0:174 offset1:239
	ds_read2_b32 v[176:177], v14 offset0:48 offset1:113
	ds_read2_b32 v[178:179], v14 offset0:178 offset1:243
	ds_read2_b32 v[180:181], v192 offset0:52 offset1:117
	ds_read2_b32 v[182:183], v192 offset0:182 offset1:247
	ds_read2_b32 v[184:185], v14 offset0:56 offset1:121
	ds_read2_b32 v[186:187], v14 offset0:186 offset1:251
	ds_read2_b32 v[188:189], v192 offset0:60 offset1:125
	ds_read2_b32 v[190:191], v192 offset0:190 offset1:255
	s_waitcnt lgkmcnt(0)
	v_add_u32_e32 v24, s59, v13
	v_mul_lo_u32 v22, s57, v24
	s_ashr_i32 s59, s58, 31
	v_readlane_b32 s76, v254, 31
	s_waitcnt lgkmcnt(0)
	v_mul_f32_e32 v8, v4, v128
	v_mul_f32_e32 v15, v5, v129
	v_cvt_pk_bf16_f32 v16, v8, v15
	s_add_i32 s3, s3, s33
	s_add_i32 s66, s66, s67
	s_add_i32 s68, s68, s69
	s_add_i32 s70, s70, s71
	s_waitcnt lgkmcnt(0)
	v_mul_f32_e32 v15, v7, v131
	v_mul_f32_e32 v8, v6, v130
	v_cvt_pk_bf16_f32 v17, v8, v15
	v_add_u32_e32 v15, 0x400, v14
	s_add_i32 s72, s72, s73
	s_add_i32 s74, s74, s75
	v_readlane_b32 s78, v254, 33
	v_readlane_b32 s79, v254, 34
	s_waitcnt lgkmcnt(0)
	v_mul_f32_e32 v8, v0, v132
	v_mul_f32_e32 v18, v1, v133
	v_cvt_pk_bf16_f32 v18, v8, v18
	v_readlane_b32 s80, v255, 21
	v_readlane_b32 s77, v254, 32
	s_movk_i32 s78, 0x1580
	v_readlane_b32 s82, v255, 23
	s_waitcnt lgkmcnt(0)
	v_mul_f32_e32 v8, v2, v134
	v_mul_f32_e32 v19, v3, v135
	v_cvt_pk_bf16_f32 v19, v8, v19
	v_ashrrev_i32_e32 v8, 31, v24
	v_mul_lo_u32 v8, s56, v8
	v_mad_u64_u32 v[20:21], s[4:5], s56, v24, 0
	v_add3_u32 v21, v21, v8, v22
	v_lshl_add_u64 v[20:21], v[20:21], 1, s[60:61]
	s_lshl_b64 s[4:5], s[58:59], 1
	v_lshl_add_u64 v[20:21], v[20:21], 0, s[4:5]
	v_lshlrev_b32_e32 v8, 1, v10
	v_lshl_add_u64 v[20:21], v[20:21], 0, v[8:9]
	global_store_dwordx4 v[20:21], v[16:19], off sc1 nt
	s_cmpk_lt_i32 s3, 25216
	v_readlane_b32 s83, v255, 24
	s_waitcnt lgkmcnt(0)
	v_mul_f32_e32 v16, v4, v136
	v_mul_f32_e32 v17, v5, v137
	v_cvt_pk_bf16_f32 v16, v16, v17
	s_mov_b32 s79, 0x3f22f983
	s_mov_b32 s85, 0xbfc90fda
	s_brev_b32 s86, 1
	s_movk_i32 s87, 0x1f8
	s_waitcnt lgkmcnt(0)
	v_mul_f32_e32 v17, v6, v138
	v_mul_f32_e32 v18, v7, v139
	v_cvt_pk_bf16_f32 v17, v17, v18
	s_mov_b64 s[88:89], 0x80
	s_mov_b64 s[92:93], 0x4000
	s_mov_b64 s[94:95], 0x4800
	v_readlane_b32 s81, v255, 22
	s_waitcnt lgkmcnt(0)
	v_mul_f32_e32 v18, v0, v140
	v_mul_f32_e32 v19, v1, v141
	v_cvt_pk_bf16_f32 v18, v18, v19
	s_waitcnt lgkmcnt(0)
	v_mul_f32_e32 v19, v2, v142
	v_mul_f32_e32 v20, v3, v143
	v_cvt_pk_bf16_f32 v19, v19, v20
	v_add_u32_e32 v20, 8, v24
	v_ashrrev_i32_e32 v21, 31, v20
	v_mul_lo_u32 v22, s56, v21
	v_mul_lo_u32 v23, s57, v20
	v_mad_u64_u32 v[20:21], s[6:7], s56, v20, 0
	v_add3_u32 v21, v21, v22, v23
	v_lshl_add_u64 v[20:21], v[20:21], 1, s[60:61]
	v_lshl_add_u64 v[20:21], v[20:21], 0, s[4:5]
	v_lshl_add_u64 v[20:21], v[20:21], 0, v[8:9]
	global_store_dwordx4 v[20:21], v[16:19], off sc1 nt
	s_waitcnt lgkmcnt(0)
	s_nop 0
	v_mul_f32_e32 v16, v4, v144
	v_mul_f32_e32 v17, v5, v145
	v_cvt_pk_bf16_f32 v16, v16, v17
	s_waitcnt lgkmcnt(0)
	v_mul_f32_e32 v17, v6, v146
	v_mul_f32_e32 v18, v7, v147
	v_cvt_pk_bf16_f32 v17, v17, v18
	s_waitcnt lgkmcnt(0)
	v_mul_f32_e32 v18, v0, v148
	v_mul_f32_e32 v19, v1, v149
	v_cvt_pk_bf16_f32 v18, v18, v19
	s_waitcnt lgkmcnt(0)
; __device__ __forceinline__ unsigned cvt_pk_bf16(float lo, float hi) { unsigned r; asm volatile("v_cvt_pk_bf16_f32 %0, %1, %2" : "=v"(r) : "v"(lo), "v"(hi)); return r; }
; #define LAS __attribute__((address_space(3)))
; __device__ __forceinline__ void conv_store(const ConvItem& ci, LAS float* scr, int lane, const float (&v)[64]) {
;     ...
;     for (int j = 0; j < 8; ++j) { const int n = (lane >> 3) + 8 * j; const LAS float* s = scr + (8 * c) * 65 + n;
;         v4u o; o.x = cvt_pk_bf16(s[0 * 65] * s0[0], s[1 * 65] * s0[1]); o.y = cvt_pk_bf16(s[2 * 65] * s0[2], s[3 * 65] * s0[3]); o.z = cvt_pk_bf16(s[4 * 65] * s1[0], s[5 * 65] * s1[1]); o.w = cvt_pk_bf16(s[6 * 65] * s1[2], s[7 * 65] * s1[3]);
;         *(v4u*)(ci.dst + (size_t)(ci.drow0 + n) * ci.ldd + ci.k0 + 8 * c) = o; }
	v_mul_f32_e32 v19, v2, v150
	v_mul_f32_e32 v20, v3, v151
	v_cvt_pk_bf16_f32 v19, v19, v20
	v_add_u32_e32 v20, 16, v24
	v_ashrrev_i32_e32 v21, 31, v20
	v_mul_lo_u32 v22, s56, v21
	v_mul_lo_u32 v23, s57, v20
	v_mad_u64_u32 v[20:21], s[6:7], s56, v20, 0
	v_add3_u32 v21, v21, v22, v23
	v_lshl_add_u64 v[20:21], v[20:21], 1, s[60:61]
	v_lshl_add_u64 v[20:21], v[20:21], 0, s[4:5]
	v_lshl_add_u64 v[20:21], v[20:21], 0, v[8:9]
	global_store_dwordx4 v[20:21], v[16:19], off sc1 nt
	s_waitcnt lgkmcnt(0)
	s_nop 0
	v_mul_f32_e32 v16, v4, v152
	v_mul_f32_e32 v17, v5, v153
	v_cvt_pk_bf16_f32 v16, v16, v17
	s_waitcnt lgkmcnt(0)
	v_mul_f32_e32 v17, v6, v154
	v_mul_f32_e32 v18, v7, v155
	v_cvt_pk_bf16_f32 v17, v17, v18
	s_waitcnt lgkmcnt(0)
	v_mul_f32_e32 v18, v0, v156
	v_mul_f32_e32 v19, v1, v157
	v_cvt_pk_bf16_f32 v18, v18, v19
	s_waitcnt lgkmcnt(0)
	v_mul_f32_e32 v19, v2, v158
	v_mul_f32_e32 v20, v3, v159
	v_cvt_pk_bf16_f32 v19, v19, v20
	v_add_u32_e32 v20, 24, v24
	v_ashrrev_i32_e32 v21, 31, v20
	v_mul_lo_u32 v22, s56, v21
	v_mul_lo_u32 v23, s57, v20
	v_mad_u64_u32 v[20:21], s[6:7], s56, v20, 0
	v_add3_u32 v21, v21, v22, v23
	v_lshl_add_u64 v[20:21], v[20:21], 1, s[60:61]
	v_lshl_add_u64 v[20:21], v[20:21], 0, s[4:5]
	v_lshl_add_u64 v[20:21], v[20:21], 0, v[8:9]
	global_store_dwordx4 v[20:21], v[16:19], off sc1 nt
	s_waitcnt lgkmcnt(0)
	s_nop 0
	v_mul_f32_e32 v16, v4, v160
	v_mul_f32_e32 v17, v5, v161
	v_cvt_pk_bf16_f32 v16, v16, v17
	s_waitcnt lgkmcnt(0)
	v_mul_f32_e32 v17, v6, v162
	v_mul_f32_e32 v18, v7, v163
	v_cvt_pk_bf16_f32 v17, v17, v18
	s_waitcnt lgkmcnt(0)
	v_mul_f32_e32 v18, v0, v164
	v_mul_f32_e32 v19, v1, v165
	v_cvt_pk_bf16_f32 v18, v18, v19
	s_waitcnt lgkmcnt(0)
	v_mul_f32_e32 v19, v2, v166
	v_mul_f32_e32 v20, v3, v167
	v_cvt_pk_bf16_f32 v19, v19, v20
	v_add_u32_e32 v20, 32, v24
	v_ashrrev_i32_e32 v21, 31, v20
	v_mul_lo_u32 v22, s56, v21
	v_mul_lo_u32 v23, s57, v20
	v_mad_u64_u32 v[20:21], s[6:7], s56, v20, 0
	v_add3_u32 v21, v21, v22, v23
	v_lshl_add_u64 v[20:21], v[20:21], 1, s[60:61]
	v_lshl_add_u64 v[20:21], v[20:21], 0, s[4:5]
	v_lshl_add_u64 v[20:21], v[20:21], 0, v[8:9]
	global_store_dwordx4 v[20:21], v[16:19], off sc1 nt
	s_waitcnt lgkmcnt(0)
	s_nop 0
	v_mul_f32_e32 v16, v4, v168
	v_mul_f32_e32 v17, v5, v169
	v_cvt_pk_bf16_f32 v16, v16, v17
	s_waitcnt lgkmcnt(0)
	v_mul_f32_e32 v17, v6, v170
	v_mul_f32_e32 v18, v7, v171
	v_cvt_pk_bf16_f32 v17, v17, v18
	s_waitcnt lgkmcnt(0)
	v_mul_f32_e32 v18, v0, v172
	v_mul_f32_e32 v19, v1, v173
	v_cvt_pk_bf16_f32 v18, v18, v19
	s_waitcnt lgkmcnt(0)
	v_mul_f32_e32 v19, v2, v174
	v_mul_f32_e32 v20, v3, v175
	v_cvt_pk_bf16_f32 v19, v19, v20
	v_add_u32_e32 v20, 40, v24
	v_ashrrev_i32_e32 v21, 31, v20
	v_mul_lo_u32 v22, s56, v21
	v_mul_lo_u32 v23, s57, v20
	v_mad_u64_u32 v[20:21], s[6:7], s56, v20, 0
	v_add3_u32 v21, v21, v22, v23
	v_lshl_add_u64 v[20:21], v[20:21], 1, s[60:61]
	v_lshl_add_u64 v[20:21], v[20:21], 0, s[4:5]
	v_lshl_add_u64 v[20:21], v[20:21], 0, v[8:9]
	global_store_dwordx4 v[20:21], v[16:19], off sc1 nt
	s_waitcnt lgkmcnt(0)
	s_nop 0
	v_mul_f32_e32 v16, v4, v176
	v_mul_f32_e32 v17, v5, v177
	v_cvt_pk_bf16_f32 v16, v16, v17
	s_waitcnt lgkmcnt(0)
	v_mul_f32_e32 v17, v6, v178
	v_mul_f32_e32 v18, v7, v179
	v_cvt_pk_bf16_f32 v17, v17, v18
	s_waitcnt lgkmcnt(0)
	v_mul_f32_e32 v18, v0, v180
	v_mul_f32_e32 v19, v1, v181
	v_cvt_pk_bf16_f32 v18, v18, v19
	s_waitcnt lgkmcnt(0)
	v_mul_f32_e32 v19, v2, v182
	v_mul_f32_e32 v20, v3, v183
	v_cvt_pk_bf16_f32 v19, v19, v20
	v_add_u32_e32 v20, 48, v24
	v_ashrrev_i32_e32 v21, 31, v20
	v_mul_lo_u32 v22, s56, v21
	v_mul_lo_u32 v23, s57, v20
	v_mad_u64_u32 v[20:21], s[6:7], s56, v20, 0
	v_add3_u32 v21, v21, v22, v23
	v_lshl_add_u64 v[20:21], v[20:21], 1, s[60:61]
	v_lshl_add_u64 v[20:21], v[20:21], 0, s[4:5]
	v_lshl_add_u64 v[20:21], v[20:21], 0, v[8:9]
	global_store_dwordx4 v[20:21], v[16:19], off sc1 nt
	s_waitcnt lgkmcnt(0)
	v_mul_f32_e32 v4, v4, v184
	v_mul_f32_e32 v5, v5, v185
	v_cvt_pk_bf16_f32 v4, v4, v5
	s_waitcnt lgkmcnt(0)
	v_mul_f32_e32 v5, v6, v186
	v_mul_f32_e32 v6, v7, v187
	v_cvt_pk_bf16_f32 v5, v5, v6
	s_waitcnt lgkmcnt(0)
	v_mul_f32_e32 v0, v0, v188
	v_mul_f32_e32 v1, v1, v189
	v_cvt_pk_bf16_f32 v6, v0, v1
	s_waitcnt lgkmcnt(0)
	v_mul_f32_e32 v0, v2, v190
	v_mul_f32_e32 v1, v3, v191
	v_cvt_pk_bf16_f32 v7, v0, v1
	v_add_u32_e32 v0, 56, v24
	v_ashrrev_i32_e32 v1, 31, v0
	v_mul_lo_u32 v2, s56, v1
	v_mul_lo_u32 v3, s57, v0
	v_mad_u64_u32 v[0:1], s[6:7], s56, v0, 0
	v_add3_u32 v1, v1, v2, v3
	v_lshl_add_u64 v[0:1], v[0:1], 1, s[60:61]
	v_lshl_add_u64 v[0:1], v[0:1], 0, s[4:5]
	v_lshl_add_u64 v[0:1], v[0:1], 0, v[8:9]
	global_store_dwordx4 v[0:1], v[4:7], off sc1 nt
	s_waitcnt lgkmcnt(0)
	s_cbranch_scc0 .Lcvp31_ret

; __device__ __forceinline__ void conv_load(const ConvItem& ci, int lane, float (&v)[64]) {
;     const bool okc = ci.srcc >= 0 && (ci.srcc + lane) < ci.ncols;
;     const float* base = ci.W + (okc ? ci.srcc + lane : 0);
;     const int kmax = ci.Ksrc - 1;
; #pragma unroll
;     for (int i = 0; i < 64; ++i) { const int k = ci.k0 + i, kk = k < kmax ? k : kmax; v[i] = __builtin_nontemporal_load(base + (size_t)kk * ci.ldw); }
; #pragma unroll
;     for (int i = 0; i < 64; ++i) v[i] = (okc && (ci.k0 + i) < ci.Ksrc) ? v[i] : 0.f;
.Lcvp130_30:
	s_cmp_lt_i32 s58, s76
	s_cselect_b64 s[4:5], -1, 0
	s_and_b64 s[4:5], vcc, s[4:5]
	s_cmp_lt_i32 s64, s76
	s_waitcnt vmcnt(62)
	v_cndmask_b32_e64 v21, 0, v21, s[4:5]
	s_cselect_b64 s[4:5], -1, 0
	s_and_b64 s[4:5], vcc, s[4:5]
	s_cmp_lt_i32 s65, s76
	v_cndmask_b32_e64 v20, 0, v20, s[4:5]
	s_cselect_b64 s[4:5], -1, 0
	s_and_b64 s[4:5], vcc, s[4:5]
	s_cmp_lt_i32 s78, s76
	s_waitcnt vmcnt(61)
	v_cndmask_b32_e64 v19, 0, v19, s[4:5]
	s_cselect_b64 s[4:5], -1, 0
	s_and_b64 s[4:5], vcc, s[4:5]
	s_cmp_lt_i32 s79, s76
	s_waitcnt vmcnt(60)
	v_cndmask_b32_e64 v18, 0, v18, s[4:5]
	s_cselect_b64 s[4:5], -1, 0
	s_and_b64 s[4:5], vcc, s[4:5]
	s_cmp_lt_i32 s80, s76
	s_waitcnt vmcnt(59)
	v_cndmask_b32_e64 v17, 0, v17, s[4:5]
	s_cselect_b64 s[4:5], -1, 0
	s_and_b64 s[4:5], vcc, s[4:5]
	s_cmp_lt_i32 s81, s76
	s_waitcnt vmcnt(58)
	v_cndmask_b32_e64 v16, 0, v16, s[4:5]
	s_cselect_b64 s[4:5], -1, 0
	s_and_b64 s[4:5], vcc, s[4:5]
	s_cmp_lt_i32 s82, s76
	s_waitcnt vmcnt(57)
	v_cndmask_b32_e64 v15, 0, v15, s[4:5]
	s_cselect_b64 s[4:5], -1, 0
	s_and_b64 s[4:5], vcc, s[4:5]
	s_cmp_lt_i32 s83, s76
	s_waitcnt vmcnt(56)
	v_cndmask_b32_e64 v8, 0, v8, s[4:5]
	s_cselect_b64 s[4:5], -1, 0
	s_and_b64 s[4:5], vcc, s[4:5]
	s_cmp_lt_i32 s85, s76
	s_waitcnt vmcnt(55)
	v_cndmask_b32_e64 v29, 0, v29, s[4:5]
	s_cselect_b64 s[4:5], -1, 0
	s_and_b64 s[4:5], vcc, s[4:5]
	s_cmp_lt_i32 s86, s76
	s_waitcnt vmcnt(54)
	v_cndmask_b32_e64 v28, 0, v28, s[4:5]
	s_cselect_b64 s[4:5], -1, 0
	s_and_b64 s[4:5], vcc, s[4:5]
	s_cmp_lt_i32 s87, s76
	s_waitcnt vmcnt(53)
	v_cndmask_b32_e64 v27, 0, v27, s[4:5]
	s_cselect_b64 s[4:5], -1, 0
	s_and_b64 s[4:5], vcc, s[4:5]
	s_cmp_lt_i32 s88, s76
	s_waitcnt vmcnt(52)
	v_cndmask_b32_e64 v26, 0, v26, s[4:5]
	s_cselect_b64 s[4:5], -1, 0
	s_and_b64 s[4:5], vcc, s[4:5]
	s_cmp_lt_i32 s89, s76
	s_waitcnt vmcnt(51)
	v_cndmask_b32_e64 v25, 0, v25, s[4:5]
	s_cselect_b64 s[4:5], -1, 0
	s_and_b64 s[4:5], vcc, s[4:5]
	s_cmp_lt_i32 s90, s76
	s_waitcnt vmcnt(50)
	v_cndmask_b32_e64 v24, 0, v24, s[4:5]
	s_cselect_b64 s[4:5], -1, 0
	s_and_b64 s[4:5], vcc, s[4:5]
	s_cmp_lt_i32 s92, s76
	s_waitcnt vmcnt(49)
	v_cndmask_b32_e64 v23, 0, v23, s[4:5]
	s_cselect_b64 s[4:5], -1, 0
	s_and_b64 s[4:5], vcc, s[4:5]
	s_cmp_lt_i32 s93, s76
	s_waitcnt vmcnt(48)
	v_cndmask_b32_e64 v22, 0, v22, s[4:5]
	s_cselect_b64 s[4:5], -1, 0
	s_and_b64 s[4:5], vcc, s[4:5]
	s_cmp_lt_i32 s94, s76
	s_waitcnt vmcnt(47)
	v_cndmask_b32_e64 v37, 0, v37, s[4:5]
	s_cselect_b64 s[4:5], -1, 0
	s_and_b64 s[4:5], vcc, s[4:5]
	s_cmp_lt_i32 s95, s76
	s_waitcnt vmcnt(46)
	v_cndmask_b32_e64 v36, 0, v36, s[4:5]
	s_cselect_b64 s[4:5], -1, 0
	s_and_b64 s[4:5], vcc, s[4:5]
	s_cmp_lt_i32 s50, s76
	s_waitcnt vmcnt(45)
	v_cndmask_b32_e64 v35, 0, v35, s[4:5]
	s_cselect_b64 s[4:5], -1, 0
	s_and_b64 s[4:5], vcc, s[4:5]
	s_cmp_lt_i32 s51, s76
	s_waitcnt vmcnt(44)
	v_cndmask_b32_e64 v34, 0, v34, s[4:5]
	s_cselect_b64 s[4:5], -1, 0
	s_and_b64 s[4:5], vcc, s[4:5]
	s_cmp_lt_i32 s52, s76
	s_waitcnt vmcnt(43)
	v_cndmask_b32_e64 v33, 0, v33, s[4:5]
	s_cselect_b64 s[4:5], -1, 0
	s_and_b64 s[4:5], vcc, s[4:5]
	s_cmp_lt_i32 s53, s76
	s_waitcnt vmcnt(42)
	v_cndmask_b32_e64 v32, 0, v32, s[4:5]
	s_cselect_b64 s[4:5], -1, 0
	s_and_b64 s[4:5], vcc, s[4:5]
	s_cmp_lt_i32 s6, s76
	s_waitcnt vmcnt(41)
	v_cndmask_b32_e64 v31, 0, v31, s[4:5]
	s_cselect_b64 s[4:5], -1, 0
	s_and_b64 s[4:5], vcc, s[4:5]
	s_cmp_lt_i32 s7, s76
	s_waitcnt vmcnt(40)
	v_cndmask_b32_e64 v30, 0, v30, s[4:5]
	s_cselect_b64 s[4:5], -1, 0
	s_and_b64 s[4:5], vcc, s[4:5]
	s_cmp_lt_i32 s8, s76
	s_waitcnt vmcnt(39)
	v_cndmask_b32_e64 v45, 0, v45, s[4:5]
	s_cselect_b64 s[4:5], -1, 0
	s_and_b64 s[4:5], vcc, s[4:5]
	s_cmp_lt_i32 s9, s76
	s_waitcnt vmcnt(38)
	v_cndmask_b32_e64 v44, 0, v44, s[4:5]
	s_cselect_b64 s[4:5], -1, 0
	s_and_b64 s[4:5], vcc, s[4:5]
	s_cmp_lt_i32 s10, s76
	s_waitcnt vmcnt(37)
	v_cndmask_b32_e64 v43, 0, v43, s[4:5]
	s_cselect_b64 s[4:5], -1, 0
	s_and_b64 s[4:5], vcc, s[4:5]
	s_cmp_lt_i32 s11, s76
	s_waitcnt vmcnt(36)
	v_cndmask_b32_e64 v42, 0, v42, s[4:5]
	s_cselect_b64 s[4:5], -1, 0
	s_and_b64 s[4:5], vcc, s[4:5]
	s_cmp_lt_i32 s14, s76
	s_waitcnt vmcnt(35)
	v_cndmask_b32_e64 v41, 0, v41, s[4:5]
	s_cselect_b64 s[4:5], -1, 0
	s_and_b64 s[4:5], vcc, s[4:5]
	s_cmp_lt_i32 s15, s76
	s_waitcnt vmcnt(34)
	v_cndmask_b32_e64 v40, 0, v40, s[4:5]
	s_cselect_b64 s[4:5], -1, 0
	s_and_b64 s[4:5], vcc, s[4:5]
	s_cmp_lt_i32 s16, s76
	s_waitcnt vmcnt(33)
	v_cndmask_b32_e64 v39, 0, v39, s[4:5]
	s_cselect_b64 s[4:5], -1, 0
	s_and_b64 s[4:5], vcc, s[4:5]
	s_cmp_lt_i32 s17, s76
	s_waitcnt vmcnt(32)
	v_cndmask_b32_e64 v38, 0, v38, s[4:5]
	s_cselect_b64 s[4:5], -1, 0
	s_and_b64 s[4:5], vcc, s[4:5]
	s_cmp_lt_i32 s12, s76
	s_waitcnt vmcnt(31)
	v_cndmask_b32_e64 v53, 0, v53, s[4:5]
	s_cselect_b64 s[4:5], -1, 0
	s_and_b64 s[4:5], vcc, s[4:5]
	s_cmp_lt_i32 s13, s76
	s_waitcnt vmcnt(30)
	v_cndmask_b32_e64 v52, 0, v52, s[4:5]
	s_cselect_b64 s[4:5], -1, 0
	s_and_b64 s[4:5], vcc, s[4:5]
	s_cmp_lt_i32 s20, s76
	s_waitcnt vmcnt(29)
	v_cndmask_b32_e64 v51, 0, v51, s[4:5]
	s_cselect_b64 s[4:5], -1, 0
	s_and_b64 s[4:5], vcc, s[4:5]
	s_cmp_lt_i32 s21, s76
	s_waitcnt vmcnt(28)
	v_cndmask_b32_e64 v50, 0, v50, s[4:5]
	s_cselect_b64 s[4:5], -1, 0
	s_and_b64 s[4:5], vcc, s[4:5]
	s_cmp_lt_i32 s24, s76
	s_waitcnt vmcnt(27)
	v_cndmask_b32_e64 v49, 0, v49, s[4:5]
	s_cselect_b64 s[4:5], -1, 0
	s_and_b64 s[4:5], vcc, s[4:5]
	s_cmp_lt_i32 s25, s76
	s_waitcnt vmcnt(26)
	v_cndmask_b32_e64 v48, 0, v48, s[4:5]
	s_cselect_b64 s[4:5], -1, 0
	s_and_b64 s[4:5], vcc, s[4:5]
	s_cmp_lt_i32 s26, s76
	s_waitcnt vmcnt(25)
	v_cndmask_b32_e64 v47, 0, v47, s[4:5]
	s_cselect_b64 s[4:5], -1, 0
	s_and_b64 s[4:5], vcc, s[4:5]
	s_cmp_lt_i32 s27, s76
	s_waitcnt vmcnt(24)
; #define LAS __attribute__((address_space(3)))
; #define LDS_WAIT() asm volatile("s_waitcnt lgkmcnt(0)" ::: "memory")
; __device__ __forceinline__ void conv_load(const ConvItem& ci, int lane, float (&v)[64]) {
;     ...
;     for (int i = 0; i < 64; ++i) v[i] = (okc && (ci.k0 + i) < ci.Ksrc) ? v[i] : 0.f;
; }
; __device__ __forceinline__ void conv_store(const ConvItem& ci, LAS float* scr, int lane, const float (&v)[64]) {
;     const int c = lane & 7;
;     f32x4 s0 = {1.f, 1.f, 1.f, 1.f}, s1 = s0;
;     if (ci.ks) { const int kb = ci.k0 + 8 * c < ci.Ksrc - 8 ? ci.k0 + 8 * c : ci.Ksrc - 8; s0 = *(const f32x4*)(ci.ks + kb); s1 = *(const f32x4*)(ci.ks + kb + 4); }
; #pragma unroll
;     for (int i = 0; i < 64; ++i) scr[i * 65 + lane] = v[i];
;     LDS_WAIT(); asm volatile("" ::: "memory");
	v_cndmask_b32_e64 v46, 0, v46, s[4:5]
	s_cselect_b64 s[4:5], -1, 0
	s_and_b64 s[4:5], vcc, s[4:5]
	s_cmp_lt_i32 s18, s76
	s_waitcnt vmcnt(23)
	v_cndmask_b32_e64 v61, 0, v61, s[4:5]
	s_cselect_b64 s[4:5], -1, 0
	s_and_b64 s[4:5], vcc, s[4:5]
	s_cmp_lt_i32 s19, s76
	s_waitcnt vmcnt(22)
	v_cndmask_b32_e64 v60, 0, v60, s[4:5]
	s_cselect_b64 s[4:5], -1, 0
	s_and_b64 s[4:5], vcc, s[4:5]
	s_cmp_lt_i32 s28, s76
	s_waitcnt vmcnt(21)
	v_cndmask_b32_e64 v59, 0, v59, s[4:5]
	s_cselect_b64 s[4:5], -1, 0
	s_and_b64 s[4:5], vcc, s[4:5]
	s_cmp_lt_i32 s29, s76
	s_waitcnt vmcnt(20)
	v_cndmask_b32_e64 v58, 0, v58, s[4:5]
	s_cselect_b64 s[4:5], -1, 0
	s_and_b64 s[4:5], vcc, s[4:5]
	s_cmp_lt_i32 s22, s76
	s_waitcnt vmcnt(19)
	v_cndmask_b32_e64 v57, 0, v57, s[4:5]
	s_cselect_b64 s[4:5], -1, 0
	s_and_b64 s[4:5], vcc, s[4:5]
	s_cmp_lt_i32 s23, s76
	s_waitcnt vmcnt(18)
	v_cndmask_b32_e64 v56, 0, v56, s[4:5]
	s_cselect_b64 s[4:5], -1, 0
	s_and_b64 s[4:5], vcc, s[4:5]
	s_cmp_lt_i32 s30, s76
	s_waitcnt vmcnt(17)
	v_cndmask_b32_e64 v55, 0, v55, s[4:5]
	s_cselect_b64 s[4:5], -1, 0
	s_and_b64 s[4:5], vcc, s[4:5]
	s_cmp_lt_i32 s31, s76
	s_waitcnt vmcnt(16)
	v_cndmask_b32_e64 v54, 0, v54, s[4:5]
	s_cselect_b64 s[4:5], -1, 0
	s_and_b64 s[4:5], vcc, s[4:5]
	s_cmp_lt_i32 s36, s76
	s_waitcnt vmcnt(15)
	v_cndmask_b32_e64 v70, 0, v70, s[4:5]
	s_cselect_b64 s[4:5], -1, 0
	s_and_b64 s[4:5], vcc, s[4:5]
	s_cmp_lt_i32 s37, s76
	s_waitcnt vmcnt(14)
	v_cndmask_b32_e64 v69, 0, v69, s[4:5]
	s_cselect_b64 s[4:5], -1, 0
	s_and_b64 s[4:5], vcc, s[4:5]
	s_cmp_lt_i32 s38, s76
	s_waitcnt vmcnt(13)
	v_cndmask_b32_e64 v68, 0, v68, s[4:5]
	s_cselect_b64 s[4:5], -1, 0
	s_and_b64 s[4:5], vcc, s[4:5]
	s_cmp_lt_i32 s39, s76
	s_waitcnt vmcnt(12)
	v_cndmask_b32_e64 v67, 0, v67, s[4:5]
	s_cselect_b64 s[4:5], -1, 0
	s_and_b64 s[4:5], vcc, s[4:5]
	s_cmp_lt_i32 s34, s76
	s_waitcnt vmcnt(11)
	v_cndmask_b32_e64 v66, 0, v66, s[4:5]
	s_cselect_b64 s[4:5], -1, 0
	s_and_b64 s[4:5], vcc, s[4:5]
	s_cmp_lt_i32 s35, s76
	s_waitcnt vmcnt(10)
	v_cndmask_b32_e64 v64, 0, v64, s[4:5]
	s_cselect_b64 s[4:5], -1, 0
	s_and_b64 s[4:5], vcc, s[4:5]
	s_cmp_lt_i32 s42, s76
	s_waitcnt vmcnt(9)
	v_cndmask_b32_e64 v63, 0, v63, s[4:5]
	s_cselect_b64 s[4:5], -1, 0
	s_and_b64 s[4:5], vcc, s[4:5]
	s_cmp_lt_i32 s43, s76
	s_waitcnt vmcnt(8)
	v_cndmask_b32_e64 v62, 0, v62, s[4:5]
	s_cselect_b64 s[4:5], -1, 0
	s_and_b64 s[4:5], vcc, s[4:5]
	s_cmp_lt_i32 s54, s76
	s_waitcnt vmcnt(7)
	v_cndmask_b32_e64 v65, 0, v65, s[4:5]
	s_cselect_b64 s[4:5], -1, 0
	s_and_b64 s[4:5], vcc, s[4:5]
	s_cmp_lt_i32 s55, s76
	s_waitcnt vmcnt(6)
	v_cndmask_b32_e64 v74, 0, v74, s[4:5]
	s_cselect_b64 s[4:5], -1, 0
	s_and_b64 s[4:5], vcc, s[4:5]
	s_cmp_lt_i32 s46, s76
	ds_write2_b32 v12, v21, v20 offset1:65
	ds_write2_b32 v12, v19, v18 offset0:130 offset1:195
	v_add_u32_e32 v18, 0x400, v12
	s_waitcnt vmcnt(5)
	v_cndmask_b32_e64 v73, 0, v73, s[4:5]
	s_cselect_b64 s[4:5], -1, 0
	ds_write2_b32 v18, v17, v16 offset0:4 offset1:69
	ds_write2_b32 v18, v15, v8 offset0:134 offset1:199
	v_add_u32_e32 v8, 0x800, v12
	s_and_b64 s[4:5], vcc, s[4:5]
	ds_write2_b32 v8, v29, v28 offset0:8 offset1:73
	ds_write2_b32 v8, v27, v26 offset0:138 offset1:203
	v_add_u32_e32 v8, 0xc00, v12
	s_cmp_lt_i32 s47, s76
	ds_write2_b32 v8, v25, v24 offset0:12 offset1:77
	ds_write2_b32 v8, v23, v22 offset0:142 offset1:207
	v_add_u32_e32 v8, 0x1000, v12
	s_waitcnt vmcnt(4)
	v_cndmask_b32_e64 v72, 0, v72, s[4:5]
	s_cselect_b64 s[4:5], -1, 0
	ds_write2_b32 v8, v37, v36 offset0:16 offset1:81
	ds_write2_b32 v8, v35, v34 offset0:146 offset1:211
	v_add_u32_e32 v8, 0x1400, v12
	s_and_b64 s[4:5], vcc, s[4:5]
	ds_write2_b32 v8, v33, v32 offset0:20 offset1:85
	ds_write2_b32 v8, v31, v30 offset0:150 offset1:215
	v_add_u32_e32 v8, 0x1800, v12
	s_cmp_lt_i32 s48, s76
	ds_write2_b32 v8, v45, v44 offset0:24 offset1:89
	ds_write2_b32 v8, v43, v42 offset0:154 offset1:219
	v_add_u32_e32 v8, 0x1c00, v12
	s_waitcnt vmcnt(3)
	v_cndmask_b32_e64 v71, 0, v71, s[4:5]
	s_cselect_b64 s[4:5], -1, 0
	ds_write2_b32 v8, v41, v40 offset0:28 offset1:93
	ds_write2_b32 v8, v39, v38 offset0:158 offset1:223
	v_add_u32_e32 v8, 0x2000, v12
	s_and_b64 s[4:5], vcc, s[4:5]
	ds_write2_b32 v8, v53, v52 offset0:32 offset1:97
	ds_write2_b32 v8, v51, v50 offset0:162 offset1:227
	v_add_u32_e32 v8, 0x2400, v12
	s_cmp_lt_i32 s49, s76
	ds_write2_b32 v8, v49, v48 offset0:36 offset1:101
	ds_write2_b32 v8, v47, v46 offset0:166 offset1:231
	v_add_u32_e32 v8, 0x2800, v12
	s_waitcnt vmcnt(2)
	v_cndmask_b32_e64 v77, 0, v77, s[4:5]
	s_cselect_b64 s[4:5], -1, 0
	ds_write2_b32 v8, v61, v60 offset0:40 offset1:105
	ds_write2_b32 v8, v59, v58 offset0:170 offset1:235
	v_add_u32_e32 v8, 0x2c00, v12
	s_and_b64 s[4:5], vcc, s[4:5]
	ds_write2_b32 v8, v57, v56 offset0:44 offset1:109
	ds_write2_b32 v8, v55, v54 offset0:174 offset1:239
	v_add_u32_e32 v8, 0x3000, v12
	s_cmp_lt_i32 s44, s76
	ds_write2_b32 v8, v70, v69 offset0:48 offset1:113
	ds_write2_b32 v8, v68, v67 offset0:178 offset1:243
	v_add_u32_e32 v8, 0x3400, v12
	s_waitcnt vmcnt(1)
	v_cndmask_b32_e64 v76, 0, v76, s[4:5]
	s_cselect_b64 s[4:5], -1, 0
	ds_write2_b32 v8, v66, v64 offset0:52 offset1:117
	ds_write2_b32 v8, v63, v62 offset0:182 offset1:247
	v_add_u32_e32 v8, 0x3800, v12
	s_and_b64 vcc, vcc, s[4:5]
	ds_write2_b32 v8, v65, v74 offset0:56 offset1:121
	ds_write2_b32 v8, v73, v72 offset0:186 offset1:251
	v_add_u32_e32 v8, 0x3c00, v12
	s_waitcnt vmcnt(0)
	v_cndmask_b32_e32 v75, 0, v75, vcc
	ds_write2_b32 v8, v71, v77 offset0:60 offset1:125
	ds_write2_b32 v8, v76, v75 offset0:190 offset1:255
	s_waitcnt lgkmcnt(0)
; __device__ __forceinline__ unsigned cvt_pk_bf16(float lo, float hi) { unsigned r; asm volatile("v_cvt_pk_bf16_f32 %0, %1, %2" : "=v"(r) : "v"(lo), "v"(hi)); return r; }
; #define LAS __attribute__((address_space(3)))
; #define LDS_WAIT() asm volatile("s_waitcnt lgkmcnt(0)" ::: "memory")
; __device__ __forceinline__ void conv_store(const ConvItem& ci, LAS float* scr, int lane, const float (&v)[64]) {
;     ...
;     LDS_WAIT(); asm volatile("" ::: "memory");
; #pragma unroll
;     for (int j = 0; j < 8; ++j) { const int n = (lane >> 3) + 8 * j; const LAS float* s = scr + (8 * c) * 65 + n;
;         v4u o; o.x = cvt_pk_bf16(s[0 * 65] * s0[0], s[1 * 65] * s0[1]); o.y = cvt_pk_bf16(s[2 * 65] * s0[2], s[3 * 65] * s0[3]); o.z = cvt_pk_bf16(s[4 * 65] * s1[0], s[5 * 65] * s1[1]); o.w = cvt_pk_bf16(s[6 * 65] * s1[2], s[7 * 65] * s1[3]);
;         *(v4u*)(ci.dst + (size_t)(ci.drow0 + n) * ci.ldd + ci.k0 + 8 * c) = o; }
	v_add_u32_e32 v192, 0x400, v14
	ds_read2_b32 v[128:129], v14 offset1:65
	ds_read2_b32 v[130:131], v14 offset0:130 offset1:195
	ds_read2_b32 v[132:133], v192 offset0:4 offset1:69
	ds_read2_b32 v[134:135], v192 offset0:134 offset1:199
	ds_read2_b32 v[136:137], v14 offset0:8 offset1:73
	ds_read2_b32 v[138:139], v14 offset0:138 offset1:203
	ds_read2_b32 v[140:141], v192 offset0:12 offset1:77
	ds_read2_b32 v[142:143], v192 offset0:142 offset1:207
	ds_read2_b32 v[144:145], v14 offset0:16 offset1:81
	ds_read2_b32 v[146:147], v14 offset0:146 offset1:211
	ds_read2_b32 v[148:149], v192 offset0:20 offset1:85
	ds_read2_b32 v[150:151], v192 offset0:150 offset1:215
	ds_read2_b32 v[152:153], v14 offset0:24 offset1:89
	ds_read2_b32 v[154:155], v14 offset0:154 offset1:219
	ds_read2_b32 v[156:157], v192 offset0:28 offset1:93
	ds_read2_b32 v[158:159], v192 offset0:158 offset1:223
	ds_read2_b32 v[160:161], v14 offset0:32 offset1:97
	ds_read2_b32 v[162:163], v14 offset0:162 offset1:227
	ds_read2_b32 v[164:165], v192 offset0:36 offset1:101
	ds_read2_b32 v[166:167], v192 offset0:166 offset1:231
	ds_read2_b32 v[168:169], v14 offset0:40 offset1:105
	ds_read2_b32 v[170:171], v14 offset0:170 offset1:235
	ds_read2_b32 v[172:173], v192 offset0:44 offset1:109
	ds_read2_b32 v[174:175], v192 offset0:174 offset1:239
	ds_read2_b32 v[176:177], v14 offset0:48 offset1:113
	ds_read2_b32 v[178:179], v14 offset0:178 offset1:243
	ds_read2_b32 v[180:181], v192 offset0:52 offset1:117
	ds_read2_b32 v[182:183], v192 offset0:182 offset1:247
	ds_read2_b32 v[184:185], v14 offset0:56 offset1:121
	ds_read2_b32 v[186:187], v14 offset0:186 offset1:251
	ds_read2_b32 v[188:189], v192 offset0:60 offset1:125
	ds_read2_b32 v[190:191], v192 offset0:190 offset1:255
	s_waitcnt lgkmcnt(0)
	v_add_u32_e32 v24, s59, v13
	v_mul_lo_u32 v22, s57, v24
	s_ashr_i32 s59, s58, 31
	v_readlane_b32 s76, v254, 31
	s_waitcnt lgkmcnt(0)
	v_mul_f32_e32 v8, v4, v128
	v_mul_f32_e32 v15, v5, v129
	v_cvt_pk_bf16_f32 v16, v8, v15
	s_add_i32 s3, s3, s33
	s_add_i32 s66, s66, s67
	s_add_i32 s68, s68, s69
	s_add_i32 s70, s70, s71
	s_waitcnt lgkmcnt(0)
	v_mul_f32_e32 v15, v7, v131
	v_mul_f32_e32 v8, v6, v130
	v_cvt_pk_bf16_f32 v17, v8, v15
	v_add_u32_e32 v15, 0x400, v14
	s_add_i32 s72, s72, s73
	s_add_i32 s74, s74, s75
	v_readlane_b32 s78, v254, 33
	v_readlane_b32 s79, v254, 34
	s_waitcnt lgkmcnt(0)
	v_mul_f32_e32 v8, v0, v132
	v_mul_f32_e32 v18, v1, v133
	v_cvt_pk_bf16_f32 v18, v8, v18
	v_readlane_b32 s80, v255, 21
	v_readlane_b32 s77, v254, 32
	s_movk_i32 s78, 0x1580
	v_readlane_b32 s82, v255, 23
	s_waitcnt lgkmcnt(0)
	v_mul_f32_e32 v8, v2, v134
	v_mul_f32_e32 v19, v3, v135
	v_cvt_pk_bf16_f32 v19, v8, v19
	v_ashrrev_i32_e32 v8, 31, v24
	v_mul_lo_u32 v8, s56, v8
	v_mad_u64_u32 v[20:21], s[4:5], s56, v24, 0
	v_add3_u32 v21, v21, v8, v22
	v_lshl_add_u64 v[20:21], v[20:21], 1, s[60:61]
	s_lshl_b64 s[4:5], s[58:59], 1
	v_lshl_add_u64 v[20:21], v[20:21], 0, s[4:5]
	v_lshlrev_b32_e32 v8, 1, v10
	v_lshl_add_u64 v[20:21], v[20:21], 0, v[8:9]
	global_store_dwordx4 v[20:21], v[16:19], off sc1 nt
	s_cmpk_lt_i32 s3, 18688
	v_readlane_b32 s83, v255, 24
	s_waitcnt lgkmcnt(0)
	v_mul_f32_e32 v16, v4, v136
	v_mul_f32_e32 v17, v5, v137
	v_cvt_pk_bf16_f32 v16, v16, v17
	s_mov_b32 s79, 0x3f22f983
	s_mov_b32 s85, 0xbfc90fda
	s_brev_b32 s86, 1
	s_movk_i32 s87, 0x1f8
	s_waitcnt lgkmcnt(0)
	v_mul_f32_e32 v17, v6, v138
	v_mul_f32_e32 v18, v7, v139
	v_cvt_pk_bf16_f32 v17, v17, v18
	s_mov_b64 s[88:89], 0x80
	s_mov_b64 s[92:93], 0x4000
	s_mov_b64 s[94:95], 0x4800
	v_readlane_b32 s81, v255, 22
	s_waitcnt lgkmcnt(0)
	v_mul_f32_e32 v18, v0, v140
	v_mul_f32_e32 v19, v1, v141
	v_cvt_pk_bf16_f32 v18, v18, v19
	s_waitcnt lgkmcnt(0)
	v_mul_f32_e32 v19, v2, v142
	v_mul_f32_e32 v20, v3, v143
	v_cvt_pk_bf16_f32 v19, v19, v20
	v_add_u32_e32 v20, 8, v24
	v_ashrrev_i32_e32 v21, 31, v20
	v_mul_lo_u32 v22, s56, v21
	v_mul_lo_u32 v23, s57, v20
	v_mad_u64_u32 v[20:21], s[6:7], s56, v20, 0
	v_add3_u32 v21, v21, v22, v23
	v_lshl_add_u64 v[20:21], v[20:21], 1, s[60:61]
	v_lshl_add_u64 v[20:21], v[20:21], 0, s[4:5]
	v_lshl_add_u64 v[20:21], v[20:21], 0, v[8:9]
	global_store_dwordx4 v[20:21], v[16:19], off sc1 nt
	s_waitcnt lgkmcnt(0)
	s_nop 0
	v_mul_f32_e32 v16, v4, v144
	v_mul_f32_e32 v17, v5, v145
	v_cvt_pk_bf16_f32 v16, v16, v17
	s_waitcnt lgkmcnt(0)
	v_mul_f32_e32 v17, v6, v146
	v_mul_f32_e32 v18, v7, v147
	v_cvt_pk_bf16_f32 v17, v17, v18
	s_waitcnt lgkmcnt(0)
	v_mul_f32_e32 v18, v0, v148
	v_mul_f32_e32 v19, v1, v149
	v_cvt_pk_bf16_f32 v18, v18, v19
	s_waitcnt lgkmcnt(0)
; __device__ __forceinline__ unsigned cvt_pk_bf16(float lo, float hi) { unsigned r; asm volatile("v_cvt_pk_bf16_f32 %0, %1, %2" : "=v"(r) : "v"(lo), "v"(hi)); return r; }
; #define LAS __attribute__((address_space(3)))
; __device__ __forceinline__ void conv_store(const ConvItem& ci, LAS float* scr, int lane, const float (&v)[64]) {
;     ...
;     for (int j = 0; j < 8; ++j) { const int n = (lane >> 3) + 8 * j; const LAS float* s = scr + (8 * c) * 65 + n;
;         v4u o; o.x = cvt_pk_bf16(s[0 * 65] * s0[0], s[1 * 65] * s0[1]); o.y = cvt_pk_bf16(s[2 * 65] * s0[2], s[3 * 65] * s0[3]); o.z = cvt_pk_bf16(s[4 * 65] * s1[0], s[5 * 65] * s1[1]); o.w = cvt_pk_bf16(s[6 * 65] * s1[2], s[7 * 65] * s1[3]);
;         *(v4u*)(ci.dst + (size_t)(ci.drow0 + n) * ci.ldd + ci.k0 + 8 * c) = o; }
	v_mul_f32_e32 v19, v2, v150
	v_mul_f32_e32 v20, v3, v151
	v_cvt_pk_bf16_f32 v19, v19, v20
	v_add_u32_e32 v20, 16, v24
	v_ashrrev_i32_e32 v21, 31, v20
	v_mul_lo_u32 v22, s56, v21
	v_mul_lo_u32 v23, s57, v20
	v_mad_u64_u32 v[20:21], s[6:7], s56, v20, 0
	v_add3_u32 v21, v21, v22, v23
	v_lshl_add_u64 v[20:21], v[20:21], 1, s[60:61]
	v_lshl_add_u64 v[20:21], v[20:21], 0, s[4:5]
	v_lshl_add_u64 v[20:21], v[20:21], 0, v[8:9]
	global_store_dwordx4 v[20:21], v[16:19], off sc1 nt
	s_waitcnt lgkmcnt(0)
	s_nop 0
	v_mul_f32_e32 v16, v4, v152
	v_mul_f32_e32 v17, v5, v153
	v_cvt_pk_bf16_f32 v16, v16, v17
	s_waitcnt lgkmcnt(0)
	v_mul_f32_e32 v17, v6, v154
	v_mul_f32_e32 v18, v7, v155
	v_cvt_pk_bf16_f32 v17, v17, v18
	s_waitcnt lgkmcnt(0)
	v_mul_f32_e32 v18, v0, v156
	v_mul_f32_e32 v19, v1, v157
	v_cvt_pk_bf16_f32 v18, v18, v19
	s_waitcnt lgkmcnt(0)
	v_mul_f32_e32 v19, v2, v158
	v_mul_f32_e32 v20, v3, v159
	v_cvt_pk_bf16_f32 v19, v19, v20
	v_add_u32_e32 v20, 24, v24
	v_ashrrev_i32_e32 v21, 31, v20
	v_mul_lo_u32 v22, s56, v21
	v_mul_lo_u32 v23, s57, v20
	v_mad_u64_u32 v[20:21], s[6:7], s56, v20, 0
	v_add3_u32 v21, v21, v22, v23
	v_lshl_add_u64 v[20:21], v[20:21], 1, s[60:61]
	v_lshl_add_u64 v[20:21], v[20:21], 0, s[4:5]
	v_lshl_add_u64 v[20:21], v[20:21], 0, v[8:9]
	global_store_dwordx4 v[20:21], v[16:19], off sc1 nt
	s_waitcnt lgkmcnt(0)
	s_nop 0
	v_mul_f32_e32 v16, v4, v160
	v_mul_f32_e32 v17, v5, v161
	v_cvt_pk_bf16_f32 v16, v16, v17
	s_waitcnt lgkmcnt(0)
	v_mul_f32_e32 v17, v6, v162
	v_mul_f32_e32 v18, v7, v163
	v_cvt_pk_bf16_f32 v17, v17, v18
	s_waitcnt lgkmcnt(0)
	v_mul_f32_e32 v18, v0, v164
	v_mul_f32_e32 v19, v1, v165
	v_cvt_pk_bf16_f32 v18, v18, v19
	s_waitcnt lgkmcnt(0)
	v_mul_f32_e32 v19, v2, v166
	v_mul_f32_e32 v20, v3, v167
	v_cvt_pk_bf16_f32 v19, v19, v20
	v_add_u32_e32 v20, 32, v24
	v_ashrrev_i32_e32 v21, 31, v20
	v_mul_lo_u32 v22, s56, v21
	v_mul_lo_u32 v23, s57, v20
	v_mad_u64_u32 v[20:21], s[6:7], s56, v20, 0
	v_add3_u32 v21, v21, v22, v23
	v_lshl_add_u64 v[20:21], v[20:21], 1, s[60:61]
	v_lshl_add_u64 v[20:21], v[20:21], 0, s[4:5]
	v_lshl_add_u64 v[20:21], v[20:21], 0, v[8:9]
	global_store_dwordx4 v[20:21], v[16:19], off sc1 nt
	s_waitcnt lgkmcnt(0)
	s_nop 0
	v_mul_f32_e32 v16, v4, v168
	v_mul_f32_e32 v17, v5, v169
	v_cvt_pk_bf16_f32 v16, v16, v17
	s_waitcnt lgkmcnt(0)
	v_mul_f32_e32 v17, v6, v170
	v_mul_f32_e32 v18, v7, v171
	v_cvt_pk_bf16_f32 v17, v17, v18
	s_waitcnt lgkmcnt(0)
	v_mul_f32_e32 v18, v0, v172
	v_mul_f32_e32 v19, v1, v173
	v_cvt_pk_bf16_f32 v18, v18, v19
	s_waitcnt lgkmcnt(0)
	v_mul_f32_e32 v19, v2, v174
	v_mul_f32_e32 v20, v3, v175
	v_cvt_pk_bf16_f32 v19, v19, v20
	v_add_u32_e32 v20, 40, v24
	v_ashrrev_i32_e32 v21, 31, v20
	v_mul_lo_u32 v22, s56, v21
	v_mul_lo_u32 v23, s57, v20
	v_mad_u64_u32 v[20:21], s[6:7], s56, v20, 0
	v_add3_u32 v21, v21, v22, v23
	v_lshl_add_u64 v[20:21], v[20:21], 1, s[60:61]
	v_lshl_add_u64 v[20:21], v[20:21], 0, s[4:5]
	v_lshl_add_u64 v[20:21], v[20:21], 0, v[8:9]
	global_store_dwordx4 v[20:21], v[16:19], off sc1 nt
	s_waitcnt lgkmcnt(0)
	s_nop 0
	v_mul_f32_e32 v16, v4, v176
	v_mul_f32_e32 v17, v5, v177
	v_cvt_pk_bf16_f32 v16, v16, v17
	s_waitcnt lgkmcnt(0)
	v_mul_f32_e32 v17, v6, v178
	v_mul_f32_e32 v18, v7, v179
	v_cvt_pk_bf16_f32 v17, v17, v18
	s_waitcnt lgkmcnt(0)
	v_mul_f32_e32 v18, v0, v180
	v_mul_f32_e32 v19, v1, v181
	v_cvt_pk_bf16_f32 v18, v18, v19
	s_waitcnt lgkmcnt(0)
	v_mul_f32_e32 v19, v2, v182
	v_mul_f32_e32 v20, v3, v183
	v_cvt_pk_bf16_f32 v19, v19, v20
	v_add_u32_e32 v20, 48, v24
	v_ashrrev_i32_e32 v21, 31, v20
	v_mul_lo_u32 v22, s56, v21
	v_mul_lo_u32 v23, s57, v20
	v_mad_u64_u32 v[20:21], s[6:7], s56, v20, 0
	v_add3_u32 v21, v21, v22, v23
	v_lshl_add_u64 v[20:21], v[20:21], 1, s[60:61]
	v_lshl_add_u64 v[20:21], v[20:21], 0, s[4:5]
	v_lshl_add_u64 v[20:21], v[20:21], 0, v[8:9]
	global_store_dwordx4 v[20:21], v[16:19], off sc1 nt
	s_waitcnt lgkmcnt(0)
	v_mul_f32_e32 v4, v4, v184
	v_mul_f32_e32 v5, v5, v185
	v_cvt_pk_bf16_f32 v4, v4, v5
	s_waitcnt lgkmcnt(0)
	v_mul_f32_e32 v5, v6, v186
	v_mul_f32_e32 v6, v7, v187
	v_cvt_pk_bf16_f32 v5, v5, v6
	s_waitcnt lgkmcnt(0)
	v_mul_f32_e32 v0, v0, v188
	v_mul_f32_e32 v1, v1, v189
	v_cvt_pk_bf16_f32 v6, v0, v1
	s_waitcnt lgkmcnt(0)
	v_mul_f32_e32 v0, v2, v190
	v_mul_f32_e32 v1, v3, v191
	v_cvt_pk_bf16_f32 v7, v0, v1
	v_add_u32_e32 v0, 56, v24
	v_ashrrev_i32_e32 v1, 31, v0
	v_mul_lo_u32 v2, s56, v1
	v_mul_lo_u32 v3, s57, v0
	v_mad_u64_u32 v[0:1], s[6:7], s56, v0, 0
	v_add3_u32 v1, v1, v2, v3
	v_lshl_add_u64 v[0:1], v[0:1], 1, s[60:61]
	v_lshl_add_u64 v[0:1], v[0:1], 0, s[4:5]
	v_lshl_add_u64 v[0:1], v[0:1], 0, v[8:9]
	global_store_dwordx4 v[0:1], v[4:7], off sc1 nt
	s_waitcnt lgkmcnt(0)
	s_cbranch_scc0 .Lcvp130_ret
